# K-loop heads aligned p2=6 +0 dwords; redundant setprio/waitcnt removed
# speedup vs baseline: 1.0051x; 1.0051x over previous
; template <class Epi, class Sched, bool ALIGN_EPI = false>
; __device__ __forceinline__ void gemm_phase(PG8_LAS unsigned char* lds, const Gemm g, const Sched& S, const Epi& E) {
;     ...
;         const char* nA = Sched::GATHER ? (const char*)g.A : (has_next ? (const char*)g.A + (size_t)nxt.pm * tstep : cA); const char* nB = has_next ? (const char*)g.Bt + nxt.boff + (size_t)nxt.pn * tstep : cB;
;         for (int t = 0; t < nt; t += 2) {
;             const bool last = (t == nt - 2);
;             const char* a1 = cA + (size_t)(t + 1) * kstep;
;             const char* a2 = last ? nA : cA + (size_t)(t + 2) * kstep; const char* b2 = last ? nB : cB + (size_t)(t + 2) * kstep;
;     ...
;         for (int a = 0; a < 2; ++a)
; #pragma unroll
;             for (int b = 0; b < 2; ++b)
; #pragma unroll
;                 for (int m = 0; m < 4; ++m)
; #pragma unroll
;                     for (int n = 0; n < 2; ++n) acc[a][b][m][n] = (f32x4){0.f, 0.f, 0.f, 0.f};
.LBB0_246:
	s_ashr_i32 s9, s8, 31
	s_lshl_b64 s[46:47], s[8:9], 20
	s_add_u32 s46, s40, s46
	s_addc_u32 s47, s41, s47
	s_and_b64 s[48:49], s[6:7], exec
	s_cselect_b32 s9, s47, s51
	s_cselect_b32 s76, s46, s50
	s_ashr_i32 s45, s44, 31
	s_lshl_b64 s[48:49], s[44:45], 20
	s_add_u32 s48, s3, s48
	s_addc_u32 s49, s35, s49
	s_and_b64 s[54:55], s[6:7], exec
	s_cselect_b32 s45, s49, s53
	s_cselect_b32 s77, s48, s52
	s_add_u32 s50, s50, 0x80080
	s_addc_u32 s51, s51, 0
	s_add_u32 s78, s52, 0x100
	v_mov_b32_e32 v2, 0
	s_addc_u32 s79, s53, 0
	s_mov_b32 s80, -2
	v_mov_b32_e32 v3, v2
	v_mov_b32_e32 v4, v2
	v_mov_b32_e32 v5, v2
	v_mov_b32_e32 v6, v2
	v_mov_b32_e32 v7, v2
	v_mov_b32_e32 v8, v2
	v_mov_b32_e32 v9, v2
	s_waitcnt vmcnt(0)
	v_mov_b32_e32 v18, v2
	v_mov_b32_e32 v19, v2
	v_mov_b32_e32 v20, v2
	v_mov_b32_e32 v21, v2
	v_mov_b32_e32 v22, v2
	v_mov_b32_e32 v23, v2
	v_mov_b32_e32 v24, v2
	v_mov_b32_e32 v25, v2
	v_mov_b32_e32 v34, v2
	v_mov_b32_e32 v35, v2
	v_mov_b32_e32 v36, v2
	v_mov_b32_e32 v37, v2
	v_mov_b32_e32 v38, v2
	v_mov_b32_e32 v39, v2
	v_mov_b32_e32 v40, v2
	v_mov_b32_e32 v41, v2
	v_mov_b32_e32 v50, v2
	v_mov_b32_e32 v51, v2
	v_mov_b32_e32 v52, v2
	v_mov_b32_e32 v53, v2
	v_mov_b32_e32 v54, v2
	v_mov_b32_e32 v55, v2
	v_mov_b32_e32 v56, v2
	v_mov_b32_e32 v57, v2
	v_mov_b32_e32 v66, v2
	v_mov_b32_e32 v67, v2
	v_mov_b32_e32 v68, v2
	v_mov_b32_e32 v69, v2
	v_mov_b32_e32 v70, v2
	v_mov_b32_e32 v71, v2
	v_mov_b32_e32 v72, v2
	v_mov_b32_e32 v73, v2
	v_mov_b32_e32 v82, v2
	v_mov_b32_e32 v83, v2
	v_mov_b32_e32 v84, v2
	v_mov_b32_e32 v85, v2
	v_mov_b32_e32 v86, v2
	v_mov_b32_e32 v87, v2
	v_mov_b32_e32 v88, v2
	v_mov_b32_e32 v89, v2
	v_mov_b32_e32 v98, v2
	v_mov_b32_e32 v99, v2
	v_mov_b32_e32 v100, v2
	v_mov_b32_e32 v101, v2
	v_mov_b32_e32 v102, v2
	v_mov_b32_e32 v103, v2
	v_mov_b32_e32 v104, v2
	v_mov_b32_e32 v105, v2
	v_mov_b32_e32 v114, v2
	v_mov_b32_e32 v115, v2
	v_mov_b32_e32 v116, v2
	v_mov_b32_e32 v117, v2
	v_mov_b32_e32 v118, v2
	v_mov_b32_e32 v119, v2
	v_mov_b32_e32 v120, v2
	v_mov_b32_e32 v121, v2
	v_mov_b32_e32 v74, v2
	v_mov_b32_e32 v75, v2
	v_mov_b32_e32 v76, v2
	v_mov_b32_e32 v77, v2
	v_mov_b32_e32 v78, v2
	v_mov_b32_e32 v79, v2
	v_mov_b32_e32 v80, v2
	v_mov_b32_e32 v81, v2
	v_mov_b32_e32 v90, v2
	v_mov_b32_e32 v91, v2
	v_mov_b32_e32 v92, v2
	v_mov_b32_e32 v93, v2
	v_mov_b32_e32 v94, v2
	v_mov_b32_e32 v95, v2
	v_mov_b32_e32 v96, v2
	v_mov_b32_e32 v97, v2
	v_mov_b32_e32 v106, v2
	v_mov_b32_e32 v107, v2
	v_mov_b32_e32 v108, v2
	v_mov_b32_e32 v109, v2
	v_mov_b32_e32 v110, v2
	v_mov_b32_e32 v111, v2
	v_mov_b32_e32 v112, v2
	v_mov_b32_e32 v113, v2
	v_mov_b32_e32 v122, v2
	v_mov_b32_e32 v123, v2
	v_mov_b32_e32 v124, v2
	v_mov_b32_e32 v125, v2
	v_mov_b32_e32 v126, v2
	v_mov_b32_e32 v127, v2
	v_mov_b32_e32 v128, v2
	v_mov_b32_e32 v129, v2
	v_mov_b32_e32 v58, v2
	v_mov_b32_e32 v59, v2
	v_mov_b32_e32 v60, v2
	v_mov_b32_e32 v61, v2
	v_mov_b32_e32 v62, v2
	v_mov_b32_e32 v63, v2
	v_mov_b32_e32 v64, v2
	v_mov_b32_e32 v65, v2
	v_mov_b32_e32 v42, v2
	v_mov_b32_e32 v43, v2
	v_mov_b32_e32 v44, v2
	v_mov_b32_e32 v45, v2
	v_mov_b32_e32 v46, v2
	v_mov_b32_e32 v47, v2
	v_mov_b32_e32 v48, v2
	v_mov_b32_e32 v49, v2
	v_mov_b32_e32 v26, v2
	v_mov_b32_e32 v27, v2
	v_mov_b32_e32 v28, v2
	v_mov_b32_e32 v29, v2
	v_mov_b32_e32 v30, v2
	v_mov_b32_e32 v31, v2
	v_mov_b32_e32 v32, v2
	v_mov_b32_e32 v33, v2
	v_mov_b32_e32 v10, v2
	v_mov_b32_e32 v11, v2
	v_mov_b32_e32 v12, v2
	v_mov_b32_e32 v13, v2
	v_mov_b32_e32 v14, v2
	v_mov_b32_e32 v15, v2
	v_mov_b32_e32 v16, v2
	v_mov_b32_e32 v17, v2
	.p2align 6

; template <class Epi, class Sched, bool ALIGN_EPI = false>
; __device__ __forceinline__ void gemm_phase(PG8_LAS unsigned char* lds, const Gemm g, const Sched& S, const Epi& E) {
;     ...
;         const char* nA = Sched::GATHER ? (const char*)g.A : (has_next ? (const char*)g.A + (size_t)nxt.pm * tstep : cA); const char* nB = has_next ? (const char*)g.Bt + nxt.boff + (size_t)nxt.pn * tstep : cB;
;         for (int t = 0; t < nt; t += 2) {
;             const bool last = (t == nt - 2);
;             const char* a1 = cA + (size_t)(t + 1) * kstep;
;             const char* a2 = last ? nA : cA + (size_t)(t + 2) * kstep; const char* b2 = last ? nB : cB + (size_t)(t + 2) * kstep;
;     ...
;         for (int a = 0; a < 2; ++a)
; #pragma unroll
;             for (int b = 0; b < 2; ++b)
; #pragma unroll
;                 for (int m = 0; m < 4; ++m)
; #pragma unroll
;                     for (int n = 0; n < 2; ++n) acc[a][b][m][n] = (f32x4){0.f, 0.f, 0.f, 0.f};
.LBB0_502:
	s_ashr_i32 s47, s46, 31
	s_lshl_b64 s[10:11], s[46:47], 20
	s_add_u32 s10, s3, s10
	s_addc_u32 s11, s35, s11
	s_and_b64 s[12:13], s[8:9], exec
	s_cselect_b32 s47, s11, s51
	s_cselect_b32 s49, s10, s50
	s_ashr_i32 s45, s44, 31
	s_lshl_b64 s[12:13], s[44:45], 20
	s_add_u32 s12, s58, s12
	s_addc_u32 s13, s59, s13
	s_and_b64 s[54:55], s[8:9], exec
	v_mov_b32_e32 v4, v2
	v_mov_b32_e32 v5, v2
	s_cselect_b32 s45, s13, s53
	s_cselect_b32 s78, s12, s52
	s_add_i32 s54, s76, s72
	v_mov_b32_e32 v3, v2
	v_mov_b64_e32 v[14:15], v[4:5]
	v_mov_b64_e32 v[18:19], v[4:5]
	v_mov_b64_e32 v[30:31], v[4:5]
	v_mov_b64_e32 v[34:35], v[4:5]
	v_mov_b64_e32 v[46:47], v[4:5]
	v_mov_b64_e32 v[50:51], v[4:5]
	v_mov_b64_e32 v[62:63], v[4:5]
	v_mov_b64_e32 v[66:67], v[4:5]
	v_mov_b64_e32 v[70:71], v[4:5]
	v_mov_b64_e32 v[74:75], v[4:5]
	v_mov_b64_e32 v[86:87], v[4:5]
	v_mov_b64_e32 v[90:91], v[4:5]
	v_mov_b64_e32 v[102:103], v[4:5]
	v_mov_b64_e32 v[106:107], v[4:5]
	v_mov_b64_e32 v[110:111], v[4:5]
	v_mov_b64_e32 v[118:119], v[4:5]
	v_mov_b64_e32 v[78:79], v[4:5]
	v_mov_b64_e32 v[82:83], v[4:5]
	v_mov_b64_e32 v[94:95], v[4:5]
	v_mov_b64_e32 v[98:99], v[4:5]
	v_mov_b64_e32 v[114:115], v[4:5]
	v_mov_b64_e32 v[122:123], v[4:5]
	v_mov_b64_e32 v[126:127], v[4:5]
	v_mov_b64_e32 v[130:131], v[4:5]
	v_mov_b64_e32 v[58:59], v[4:5]
	v_mov_b64_e32 v[54:55], v[4:5]
	v_mov_b64_e32 v[42:43], v[4:5]
	v_mov_b64_e32 v[38:39], v[4:5]
	v_mov_b64_e32 v[26:27], v[4:5]
	v_mov_b64_e32 v[22:23], v[4:5]
	v_mov_b64_e32 v[10:11], v[4:5]
	s_add_u32 s79, s52, 0x100
	v_mov_b64_e32 v[12:13], v[2:3]
	v_mov_b64_e32 v[16:17], v[2:3]
	v_mov_b64_e32 v[28:29], v[2:3]
	v_mov_b64_e32 v[32:33], v[2:3]
	v_mov_b64_e32 v[44:45], v[2:3]
	v_mov_b64_e32 v[48:49], v[2:3]
	v_mov_b64_e32 v[60:61], v[2:3]
	v_mov_b64_e32 v[64:65], v[2:3]
	v_mov_b64_e32 v[68:69], v[2:3]
	v_mov_b64_e32 v[72:73], v[2:3]
	v_mov_b64_e32 v[84:85], v[2:3]
	v_mov_b64_e32 v[88:89], v[2:3]
	v_mov_b64_e32 v[100:101], v[2:3]
	v_mov_b64_e32 v[104:105], v[2:3]
	v_mov_b64_e32 v[108:109], v[2:3]
	v_mov_b64_e32 v[116:117], v[2:3]
	v_mov_b64_e32 v[76:77], v[2:3]
	v_mov_b64_e32 v[80:81], v[2:3]
	v_mov_b64_e32 v[92:93], v[2:3]
	v_mov_b64_e32 v[96:97], v[2:3]
	v_mov_b64_e32 v[112:113], v[2:3]
	v_mov_b64_e32 v[120:121], v[2:3]
	v_mov_b64_e32 v[124:125], v[2:3]
	v_mov_b64_e32 v[128:129], v[2:3]
	v_mov_b64_e32 v[56:57], v[2:3]
	v_mov_b64_e32 v[52:53], v[2:3]
	v_mov_b64_e32 v[40:41], v[2:3]
	v_mov_b64_e32 v[36:37], v[2:3]
	v_mov_b64_e32 v[24:25], v[2:3]
	v_mov_b64_e32 v[20:21], v[2:3]
	v_mov_b64_e32 v[8:9], v[2:3]
	v_mov_b64_e32 v[6:7], v[4:5]
	v_add_u32_e32 v137, s54, v176
	v_lshl_add_u64 v[132:133], s[50:51], 0, v[154:155]
	v_lshl_add_u64 v[134:135], s[50:51], 0, v[156:157]
	s_addc_u32 s80, s53, 0
	s_mov_b32 s81, 0
	s_mov_b64 s[52:53], 0
	v_mov_b64_e32 v[4:5], v[2:3]
	s_branch .LBB0_504
	.p2align 6

;     __device__ __forceinline__ int arow(const Unit& u, int r) const { if (!GATHER_) return u.pm * BM + r; int slot = u.s0 + r; slot = slot < u.cnt ? slot : u.cnt - 1; return list[u.e * 16384 + slot] >> 1; }
; #define PG8_STAGE(bufoff, gbase, voff) do { _Pragma("unroll") for (int _i = 0; _i < 2; ++_i) \
;         __builtin_amdgcn_global_load_lds((const unsigned*)((const char*)(gbase) + (voff)[_i]), (PG8_LAS unsigned*)(lds + (bufoff) + ldsw + _i * 8192), 16, 0, 0); } while (0)
; template <class Epi, class Sched, bool ALIGN_EPI = false>
; __device__ __forceinline__ void gemm_phase(PG8_LAS unsigned char* lds, const Gemm g, const Sched& S, const Epi& E) {
;     ...
;     f32x4 acc[2][2][4][2];
; #pragma unroll
;     for (int a = 0; a < 2; ++a)
; #pragma unroll
;         for (int b = 0; b < 2; ++b)
; #pragma unroll
;             for (int m = 0; m < 4; ++m)
; #pragma unroll
;                 for (int n = 0; n < 2; ++n) acc[a][b][m][n] = (f32x4){0.f, 0.f, 0.f, 0.f};
;     bf16x8 At[4][2], B0[2][2], B1[2][2];
;     unsigned vc0[2], vc1[2], vn0[2], vn1[2];
;     if constexpr (Sched::GATHER) {
; #pragma unroll
;         for (int i = 0; i < 2; ++i) { vc0[i] = (unsigned)(S.arow(cur, RA[i]) * K + CA[i]) * 2u; vc1[i] = (unsigned)(S.arow(cur, RA[i] + HALF) * K + CA[i]) * 2u; vn0[i] = vc0[i]; vn1[i] = vc1[i]; }
;     } else {
; #pragma unroll
;         for (int i = 0; i < 2; ++i) { vc0[i] = voffA[i]; vc1[i] = voffA[i]; vn0[i] = voffA[i]; vn1[i] = voffA[i]; }
;     }
;     const char* cA = Sched::GATHER ? (const char*)g.A : (const char*)g.A + (size_t)cur.pm * tstep; const char* cB = (const char*)g.Bt + cur.boff + (size_t)cur.pn * tstep;
;     S.a_ready(cur);
;     PG8_STAGE(PG8_SB(0, 0), cB, voffB); PG8_STAGE(PG8_SB(0, 1), cB + hstep, voffB); PG8_STAGE(PG8_SA(0, 0), cA, vc0); PG8_STAGE(PG8_SA(0, 1), cA + hstepA, vc1);
.LBB0_720:
	v_mov_b32_e32 v153, v135
	v_mov_b32_e32 v155, v135
	s_add_u32 s49, s56, 0x100
	v_mov_b32_e32 v26, 0
	s_addc_u32 s89, s57, 0
	v_lshl_add_u64 v[158:159], s[40:41], 0, v[154:155]
	v_lshl_add_u64 v[160:161], s[40:41], 0, v[152:153]
	s_mov_b32 s90, -2
	s_mov_b64 s[56:57], 0
	v_mov_b32_e32 v27, v26
	v_mov_b32_e32 v28, v26
	v_mov_b32_e32 v29, v26
	v_mov_b32_e32 v38, v26
	v_mov_b32_e32 v39, v26
	v_mov_b32_e32 v40, v26
	v_mov_b32_e32 v41, v26
	v_mov_b32_e32 v46, v26
	v_mov_b32_e32 v47, v26
	v_mov_b32_e32 v48, v26
	v_mov_b32_e32 v49, v26
	v_mov_b32_e32 v54, v26
	v_mov_b32_e32 v55, v26
	v_mov_b32_e32 v56, v26
	v_mov_b32_e32 v57, v26
	v_mov_b32_e32 v2, v26
	v_mov_b32_e32 v3, v26
	v_mov_b32_e32 v4, v26
	v_mov_b32_e32 v5, v26
	v_mov_b32_e32 v14, v26
	v_mov_b32_e32 v15, v26
	v_mov_b32_e32 v16, v26
	v_mov_b32_e32 v17, v26
	v_mov_b32_e32 v30, v26
	v_mov_b32_e32 v31, v26
	v_mov_b32_e32 v32, v26
	v_mov_b32_e32 v33, v26
	v_mov_b32_e32 v34, v26
	v_mov_b32_e32 v35, v26
	v_mov_b32_e32 v36, v26
	v_mov_b32_e32 v37, v26
	v_mov_b32_e32 v42, v26
	v_mov_b32_e32 v43, v26
	v_mov_b32_e32 v44, v26
	v_mov_b32_e32 v45, v26
	v_mov_b32_e32 v50, v26
	v_mov_b32_e32 v51, v26
	v_mov_b32_e32 v52, v26
	v_mov_b32_e32 v53, v26
	v_mov_b32_e32 v58, v26
	v_mov_b32_e32 v59, v26
	v_mov_b32_e32 v60, v26
	v_mov_b32_e32 v61, v26
	v_mov_b32_e32 v62, v26
	v_mov_b32_e32 v63, v26
	v_mov_b32_e32 v64, v26
	v_mov_b32_e32 v65, v26
	v_mov_b32_e32 v66, v26
	v_mov_b32_e32 v67, v26
	v_mov_b32_e32 v68, v26
	v_mov_b32_e32 v69, v26
	v_mov_b32_e32 v70, v26
	v_mov_b32_e32 v71, v26
	v_mov_b32_e32 v72, v26
	v_mov_b32_e32 v73, v26
	v_mov_b32_e32 v82, v26
	v_mov_b32_e32 v83, v26
	v_mov_b32_e32 v84, v26
	v_mov_b32_e32 v85, v26
	v_mov_b32_e32 v86, v26
	v_mov_b32_e32 v87, v26
	v_mov_b32_e32 v88, v26
	v_mov_b32_e32 v89, v26
	v_mov_b32_e32 v98, v26
	v_mov_b32_e32 v99, v26
	v_mov_b32_e32 v100, v26
	v_mov_b32_e32 v101, v26
	v_mov_b32_e32 v102, v26
	v_mov_b32_e32 v103, v26
	v_mov_b32_e32 v104, v26
	v_mov_b32_e32 v105, v26
	v_mov_b32_e32 v114, v26
	v_mov_b32_e32 v115, v26
	v_mov_b32_e32 v116, v26
	v_mov_b32_e32 v117, v26
	v_mov_b32_e32 v118, v26
	v_mov_b32_e32 v119, v26
	v_mov_b32_e32 v120, v26
	v_mov_b32_e32 v121, v26
	v_mov_b32_e32 v74, v26
	v_mov_b32_e32 v75, v26
	v_mov_b32_e32 v76, v26
	v_mov_b32_e32 v77, v26
	v_mov_b32_e32 v78, v26
	v_mov_b32_e32 v79, v26
	v_mov_b32_e32 v80, v26
	v_mov_b32_e32 v81, v26
	v_mov_b32_e32 v90, v26
	v_mov_b32_e32 v91, v26
	v_mov_b32_e32 v92, v26
	v_mov_b32_e32 v93, v26
	v_mov_b32_e32 v94, v26
	v_mov_b32_e32 v95, v26
	v_mov_b32_e32 v96, v26
	v_mov_b32_e32 v97, v26
	v_mov_b32_e32 v106, v26
	v_mov_b32_e32 v107, v26
	v_mov_b32_e32 v108, v26
	v_mov_b32_e32 v109, v26
	v_mov_b32_e32 v110, v26
	v_mov_b32_e32 v111, v26
	v_mov_b32_e32 v112, v26
	v_mov_b32_e32 v113, v26
	v_mov_b32_e32 v122, v26
	v_mov_b32_e32 v123, v26
	v_mov_b32_e32 v124, v26
	v_mov_b32_e32 v125, v26
	v_mov_b32_e32 v126, v26
	v_mov_b32_e32 v127, v26
	v_mov_b32_e32 v128, v26
	v_mov_b32_e32 v129, v26
	v_mov_b32_e32 v22, v26
	v_mov_b32_e32 v23, v26
	v_mov_b32_e32 v24, v26
	v_mov_b32_e32 v25, v26
	v_mov_b32_e32 v18, v26
	v_mov_b32_e32 v19, v26
	v_mov_b32_e32 v20, v26
	v_mov_b32_e32 v21, v26
	v_mov_b32_e32 v10, v26
	v_mov_b32_e32 v11, v26
	v_mov_b32_e32 v12, v26
	v_mov_b32_e32 v13, v26
	v_mov_b32_e32 v6, v26
	v_mov_b32_e32 v7, v26
	v_mov_b32_e32 v8, v26
	v_mov_b32_e32 v9, v26
	.p2align 6

; #define PG8_STAGE(bufoff, gbase, voff) do { _Pragma("unroll") for (int _i = 0; _i < 2; ++_i) \
;         __builtin_amdgcn_global_load_lds((const unsigned*)((const char*)(gbase) + (voff)[_i]), (PG8_LAS unsigned*)(lds + (bufoff) + ldsw + _i * 8192), 16, 0, 0); } while (0)
; #define PG8_WAIT_V(n) asm volatile("s_waitcnt vmcnt(" #n ")" ::: "memory")
; #define PG8_BAR __builtin_amdgcn_s_barrier()
;     __device__ __forceinline__ Pre pre(const Unit& u, int wr, int fr) const { Pre p; const int rl0 = wr * 64 + fr;
; #pragma unroll
;         for (int ai = 0; ai < 2; ++ai)
; #pragma unroll
;             for (int m = 0; m < 4; ++m) { int slot = u.s0 + rl0 + ai * HALF + m * 16; slot = slot < u.cnt ? slot : u.cnt - 1; p.rs[ai][m] = lrs[u.e * 16384 + slot]; }
;         return p; }
; template <class Epi, class Sched, bool ALIGN_EPI = false>
; __device__ __forceinline__ void gemm_phase(PG8_LAS unsigned char* lds, const Gemm g, const Sched& S, const Epi& E) {
;     ...
;     PG8_STAGE(PG8_SB(0, 0), cB, voffB); PG8_STAGE(PG8_SB(0, 1), cB + hstep, voffB); PG8_STAGE(PG8_SA(0, 0), cA, vc0); PG8_STAGE(PG8_SA(0, 1), cA + hstepA, vc1);
;     if (wr == 1) PG8_BAR;
;     PG8_WAIT_V(2); PG8_BAR;
;     PG8_STAGE(PG8_SB(1, 0), cB + kstep, voffB); PG8_STAGE(PG8_SA(1, 0), cA + kstep, vc0); PG8_STAGE(PG8_SB(1, 1), cB + hstep + kstep, voffB);
;     PG8_WAIT_V(6); PG8_BAR;
;     for (;;) {
;         typename Epi::Pre pf;
;         if constexpr (Epi::KSCALE) pf = E.pre2(cur, lds, ui, tid); else pf = E.pre(cur, wr, fr);
;         const bool has_next = S.next(ui + 1, nxt);
.LBB0_786:
	s_add_u32 s22, s36, 0x30800000
	v_lshlrev_b32_e32 v9, 2, v162
	s_addc_u32 s23, s37, 0
	v_lshl_or_b32 v166, s15, 6, v162
	v_lshl_or_b32 v8, v162, 6, v163
	s_lshl_b32 s15, s15, 13
	v_and_b32_e32 v9, 32, v9
	s_lshl_b32 s14, s14, 5
	v_bitop3_b32 v20, v8, s15, v9 bitop3:0xde
	s_and_b32 s42, s14, 0x60
	s_mov_b64 s[14:15], 0x80
	s_add_i32 m0, s27, 0x18000
	v_lshl_add_u64 v[4:5], v[4:5], 0, s[14:15]
	s_waitcnt vmcnt(2)
	s_barrier
	global_load_lds_dwordx4 v[4:5], off
	s_add_i32 m0, s27, 0x1a000
	s_add_u32 s50, s36, 0x3c800080
	v_lshl_add_u64 v[2:3], v[2:3], 0, s[14:15]
	s_addc_u32 s51, s37, 0
	s_add_i32 s43, s27, 0x8000
	global_load_lds_dwordx4 v[2:3], off
	v_lshl_add_u64 v[2:3], s[50:51], 0, v[148:149]
	s_mov_b32 m0, s43
	s_add_i32 s44, s27, 0xa000
	global_load_lds_dwordx4 v[2:3], off
	v_lshl_add_u64 v[2:3], s[50:51], 0, v[150:151]
	s_add_u32 s50, s12, 0x80080
	s_mov_b32 m0, s44
	s_addc_u32 s51, s13, 0
	global_load_lds_dwordx4 v[2:3], off
	s_add_i32 m0, s27, 0x1c000
	v_lshl_add_u64 v[2:3], s[50:51], 0, v[146:147]
	global_load_lds_dwordx4 v[2:3], off
	v_lshl_add_u64 v[2:3], s[50:51], 0, v[144:145]
	s_add_i32 m0, s27, 0x1e000
	v_add_u32_e32 v18, s48, v166
	global_load_lds_dwordx4 v[2:3], off
	v_min_i32_e32 v2, s46, v18
	v_add_u32_e32 v4, 16, v18
	v_add_u32_e32 v8, 32, v18
	v_add_u32_e32 v10, 48, v18
	v_add_u32_e32 v12, 0x80, v18
	v_add_u32_e32 v14, 0x90, v18
	v_add_u32_e32 v16, 0xa0, v18
	v_add_u32_e32 v18, 0xb0, v18
	v_add_u32_e32 v2, s45, v2
	v_min_i32_e32 v4, s46, v4
	v_min_i32_e32 v8, s46, v8
	v_min_i32_e32 v10, s46, v10
	v_min_i32_e32 v12, s46, v12
	v_min_i32_e32 v14, s46, v14
	v_min_i32_e32 v16, s46, v16
	v_min_i32_e32 v18, s46, v18
	v_ashrrev_i32_e32 v3, 31, v2
	v_add_u32_e32 v4, s45, v4
	v_add_u32_e32 v8, s45, v8
	v_add_u32_e32 v10, s45, v10
	v_add_u32_e32 v12, s45, v12
	v_add_u32_e32 v14, s45, v14
	v_add_u32_e32 v16, s45, v16
	v_add_u32_e32 v18, s45, v18
	v_lshl_add_u64 v[2:3], v[2:3], 2, s[22:23]
	v_ashrrev_i32_e32 v5, 31, v4
	v_ashrrev_i32_e32 v9, 31, v8
	v_ashrrev_i32_e32 v11, 31, v10
	v_ashrrev_i32_e32 v13, 31, v12
	v_ashrrev_i32_e32 v15, 31, v14
	v_ashrrev_i32_e32 v17, 31, v16
	v_ashrrev_i32_e32 v19, 31, v18
	s_waitcnt vmcnt(6)
	s_barrier
	v_lshl_add_u64 v[4:5], v[4:5], 2, s[22:23]
	v_lshl_add_u64 v[8:9], v[8:9], 2, s[22:23]
	v_lshl_add_u64 v[10:11], v[10:11], 2, s[22:23]
	v_lshl_add_u64 v[12:13], v[12:13], 2, s[22:23]
	v_lshl_add_u64 v[14:15], v[14:15], 2, s[22:23]
	v_lshl_add_u64 v[16:17], v[16:17], 2, s[22:23]
	v_lshl_add_u64 v[18:19], v[18:19], 2, s[22:23]
	global_load_dword v156, v[2:3], off
	global_load_dword v142, v[4:5], off
	global_load_dword v140, v[8:9], off
	global_load_dword v138, v[10:11], off
	global_load_dword v136, v[12:13], off
	global_load_dword v134, v[14:15], off
	global_load_dword v132, v[16:17], off
	global_load_dword v130, v[18:19], off
	s_add_u32 s16, s16, s47
	s_addc_u32 s17, s17, 0
	s_add_u32 s45, s16, 0x4800100
	v_lshl_or_b32 v21, s42, 7, v164
	s_mov_b64 s[18:19], 0x3c800080
	s_addc_u32 s46, s17, 0
	v_add3_u32 v2, v1, v7, v141
	v_mov_b32_e32 v3, v147
	s_add_i32 s50, 0, 0x10000
	s_add_i32 s52, 0, 0x14000
	s_add_i32 s54, 0, 0x18000
	s_add_i32 s16, 0, 0x1c000
	v_lshl_add_u64 v[158:159], v[2:3], 0, s[18:19]
	v_add3_u32 v2, v1, v6, v141
	v_add_u32_e32 v167, s50, v21
	v_add_u32_e32 v168, s52, v21
	s_add_i32 s50, s50, s56
	s_add_i32 s52, s52, s56
	v_add_u32_e32 v170, s54, v21
	s_add_i32 s54, s54, s56
	s_add_i32 s56, s16, s56
	v_mov_b32_e32 v153, v147
	v_mov_b32_e32 v155, v147
	v_lshl_add_u64 v[160:161], v[2:3], 0, s[18:19]
	s_mov_b32 s47, -2
	v_add_u32_e32 v169, 0, v20
	s_add_i32 s48, s27, 0xc000
	s_add_i32 s49, s27, 0xe000
	s_add_i32 s51, s50, 0x2000
	s_add_i32 s53, s52, 0x2000
	v_add_u32_e32 v171, s16, v21
	s_add_i32 s55, s54, 0x2000
	s_add_i32 s57, s56, 0x2000
	s_mov_b64 s[16:17], s[36:37]
	v_mov_b32_e32 v30, v147
	v_mov_b32_e32 v31, v147
	v_mov_b32_e32 v32, v147
	v_mov_b32_e32 v33, v147
	v_mov_b32_e32 v38, v147
	v_mov_b32_e32 v39, v147
	v_mov_b32_e32 v40, v147
	v_mov_b32_e32 v41, v147
	v_mov_b32_e32 v46, v147
	v_mov_b32_e32 v47, v147
	v_mov_b32_e32 v48, v147
	v_mov_b32_e32 v49, v147
	v_mov_b32_e32 v54, v147
	v_mov_b32_e32 v55, v147
	v_mov_b32_e32 v56, v147
	v_mov_b32_e32 v57, v147
	v_mov_b32_e32 v2, v147
	v_mov_b32_e32 v4, v147
	v_mov_b32_e32 v5, v147
	v_mov_b32_e32 v14, v147
	v_mov_b32_e32 v15, v147
	v_mov_b32_e32 v16, v147
	v_mov_b32_e32 v17, v147
	v_mov_b32_e32 v26, v147
	v_mov_b32_e32 v27, v147
	v_mov_b32_e32 v28, v147
	v_mov_b32_e32 v29, v147
	v_mov_b32_e32 v34, v147
	v_mov_b32_e32 v35, v147
	v_mov_b32_e32 v36, v147
	v_mov_b32_e32 v37, v147
	v_mov_b32_e32 v42, v147
	v_mov_b32_e32 v43, v147
	v_mov_b32_e32 v44, v147
	v_mov_b32_e32 v45, v147
	v_mov_b32_e32 v50, v147
	v_mov_b32_e32 v51, v147
	v_mov_b32_e32 v52, v147
	v_mov_b32_e32 v53, v147
	v_mov_b32_e32 v58, v147
	v_mov_b32_e32 v59, v147
	v_mov_b32_e32 v60, v147
	v_mov_b32_e32 v61, v147
	v_mov_b32_e32 v62, v147
	v_mov_b32_e32 v63, v147
	v_mov_b32_e32 v64, v147
	v_mov_b32_e32 v65, v147
	v_mov_b32_e32 v66, v147
	v_mov_b32_e32 v67, v147
	v_mov_b32_e32 v68, v147
	v_mov_b32_e32 v69, v147
	v_mov_b32_e32 v70, v147
	v_mov_b32_e32 v71, v147
	v_mov_b32_e32 v72, v147
	v_mov_b32_e32 v73, v147
	v_mov_b32_e32 v82, v147
	v_mov_b32_e32 v83, v147
	v_mov_b32_e32 v84, v147
	v_mov_b32_e32 v85, v147
	v_mov_b32_e32 v86, v147
	v_mov_b32_e32 v87, v147
	v_mov_b32_e32 v88, v147
	v_mov_b32_e32 v89, v147
	v_mov_b32_e32 v98, v147
	v_mov_b32_e32 v99, v147
	v_mov_b32_e32 v100, v147
	v_mov_b32_e32 v101, v147
	v_mov_b32_e32 v102, v147
	v_mov_b32_e32 v103, v147
	v_mov_b32_e32 v104, v147
	v_mov_b32_e32 v105, v147
	v_mov_b32_e32 v114, v147
	v_mov_b32_e32 v115, v147
	v_mov_b32_e32 v116, v147
	v_mov_b32_e32 v117, v147
	v_mov_b32_e32 v118, v147
	v_mov_b32_e32 v119, v147
	v_mov_b32_e32 v120, v147
	v_mov_b32_e32 v121, v147
	v_mov_b32_e32 v74, v147
	v_mov_b32_e32 v75, v147
	v_mov_b32_e32 v76, v147
	v_mov_b32_e32 v77, v147
	v_mov_b32_e32 v78, v147
	v_mov_b32_e32 v79, v147
	v_mov_b32_e32 v80, v147
	v_mov_b32_e32 v81, v147
	v_mov_b32_e32 v90, v147
	v_mov_b32_e32 v91, v147
	v_mov_b32_e32 v92, v147
	v_mov_b32_e32 v93, v147
	v_mov_b32_e32 v94, v147
	v_mov_b32_e32 v95, v147
	v_mov_b32_e32 v96, v147
	v_mov_b32_e32 v97, v147
	v_mov_b32_e32 v106, v147
	v_mov_b32_e32 v107, v147
	v_mov_b32_e32 v108, v147
	v_mov_b32_e32 v109, v147
	v_mov_b32_e32 v110, v147
	v_mov_b32_e32 v111, v147
	v_mov_b32_e32 v112, v147
	v_mov_b32_e32 v113, v147
	v_mov_b32_e32 v122, v147
	v_mov_b32_e32 v123, v147
	v_mov_b32_e32 v124, v147
	v_mov_b32_e32 v125, v147
	v_mov_b32_e32 v126, v147
	v_mov_b32_e32 v127, v147
	v_mov_b32_e32 v128, v147
	v_mov_b32_e32 v129, v147
	v_mov_b32_e32 v22, v147
	v_mov_b32_e32 v23, v147
	v_mov_b32_e32 v24, v147
	v_mov_b32_e32 v25, v147
	v_mov_b32_e32 v18, v147
	v_mov_b32_e32 v19, v147
	v_mov_b32_e32 v20, v147
	v_mov_b32_e32 v21, v147
	v_mov_b32_e32 v10, v147
	v_mov_b32_e32 v11, v147
	v_mov_b32_e32 v12, v147
	v_mov_b32_e32 v13, v147
	v_mov_b32_e32 v6, v147
	v_mov_b32_e32 v7, v147
	v_mov_b32_e32 v8, v147
	v_mov_b32_e32 v9, v147
	.p2align 6

; template <class Epi, class Sched, bool ALIGN_EPI = false>
; __device__ __forceinline__ void gemm_phase(PG8_LAS unsigned char* lds, const Gemm g, const Sched& S, const Epi& E) {
;     ...
;         const char* nA = Sched::GATHER ? (const char*)g.A : (has_next ? (const char*)g.A + (size_t)nxt.pm * tstep : cA); const char* nB = has_next ? (const char*)g.Bt + nxt.boff + (size_t)nxt.pn * tstep : cB;
;         for (int t = 0; t < nt; t += 2) {
;             const bool last = (t == nt - 2);
;             const char* a1 = cA + (size_t)(t + 1) * kstep;
;             const char* a2 = last ? nA : cA + (size_t)(t + 2) * kstep; const char* b2 = last ? nB : cB + (size_t)(t + 2) * kstep;
;     ...
;         for (int a = 0; a < 2; ++a)
; #pragma unroll
;             for (int b = 0; b < 2; ++b)
; #pragma unroll
;                 for (int m = 0; m < 4; ++m)
; #pragma unroll
;                     for (int n = 0; n < 2; ++n) acc[a][b][m][n] = (f32x4){0.f, 0.f, 0.f, 0.f};
.LBB0_804:
	s_ashr_i32 s45, s44, 31
	s_lshl_b64 s[52:53], s[44:45], 18
	s_add_u32 s52, s6, s52
	s_addc_u32 s53, s7, s53
	s_and_b64 s[54:55], s[50:51], exec
	s_cselect_b32 s45, s53, s63
	s_cselect_b32 s57, s52, s62
	s_add_u32 s64, s3, s48
	s_addc_u32 s65, s35, s49
	s_ashr_i32 s47, s46, 31
	s_lshl_b64 s[54:55], s[46:47], 18
	s_add_u32 s54, s64, s54
	s_addc_u32 s55, s65, s55
	s_and_b64 s[64:65], s[50:51], exec
	s_cselect_b32 s47, s55, s61
	s_cselect_b32 s89, s54, s60
	s_add_u32 s90, s60, 0x100
	s_addc_u32 s91, s61, 0
	s_add_u32 s60, s62, 0x20080
	v_mov_b32_e32 v2, 0
	s_addc_u32 s61, s63, 0
	s_mov_b32 s92, -2
	v_mov_b32_e32 v3, v2
	v_mov_b32_e32 v4, v2
	v_mov_b32_e32 v5, v2
	v_mov_b32_e32 v6, v2
	v_mov_b32_e32 v7, v2
	v_mov_b32_e32 v8, v2
	v_mov_b32_e32 v9, v2
	v_mov_b32_e32 v10, v2
	v_mov_b32_e32 v11, v2
	v_mov_b32_e32 v12, v2
	v_mov_b32_e32 v13, v2
	v_mov_b32_e32 v14, v2
	v_mov_b32_e32 v15, v2
	v_mov_b32_e32 v16, v2
	v_mov_b32_e32 v17, v2
	v_mov_b32_e32 v26, v2
	v_mov_b32_e32 v27, v2
	v_mov_b32_e32 v28, v2
	v_mov_b32_e32 v29, v2
	v_mov_b32_e32 v30, v2
	v_mov_b32_e32 v31, v2
	v_mov_b32_e32 v32, v2
	v_mov_b32_e32 v33, v2
	v_mov_b32_e32 v42, v2
	v_mov_b32_e32 v43, v2
	v_mov_b32_e32 v44, v2
	v_mov_b32_e32 v45, v2
	v_mov_b32_e32 v54, v2
	v_mov_b32_e32 v55, v2
	v_mov_b32_e32 v56, v2
	v_mov_b32_e32 v57, v2
	v_mov_b32_e32 v58, v2
	v_mov_b32_e32 v59, v2
	v_mov_b32_e32 v60, v2
	v_mov_b32_e32 v61, v2
	v_mov_b32_e32 v62, v2
	v_mov_b32_e32 v63, v2
	v_mov_b32_e32 v64, v2
	v_mov_b32_e32 v65, v2
	v_mov_b32_e32 v78, v2
	v_mov_b32_e32 v79, v2
	v_mov_b32_e32 v80, v2
	v_mov_b32_e32 v81, v2
	v_mov_b32_e32 v86, v2
	v_mov_b32_e32 v87, v2
	v_mov_b32_e32 v88, v2
	v_mov_b32_e32 v89, v2
	v_mov_b32_e32 v94, v2
	v_mov_b32_e32 v95, v2
	v_mov_b32_e32 v96, v2
	v_mov_b32_e32 v97, v2
	v_mov_b32_e32 v102, v2
	v_mov_b32_e32 v103, v2
	v_mov_b32_e32 v104, v2
	v_mov_b32_e32 v105, v2
	v_mov_b32_e32 v110, v2
	v_mov_b32_e32 v111, v2
	v_mov_b32_e32 v112, v2
	v_mov_b32_e32 v113, v2
	v_mov_b32_e32 v118, v2
	v_mov_b32_e32 v119, v2
	v_mov_b32_e32 v120, v2
	v_mov_b32_e32 v121, v2
	v_mov_b32_e32 v74, v2
	v_mov_b32_e32 v75, v2
	v_mov_b32_e32 v76, v2
	v_mov_b32_e32 v77, v2
	v_mov_b32_e32 v82, v2
	v_mov_b32_e32 v83, v2
	v_mov_b32_e32 v84, v2
	v_mov_b32_e32 v85, v2
	v_mov_b32_e32 v90, v2
	v_mov_b32_e32 v91, v2
	v_mov_b32_e32 v92, v2
	v_mov_b32_e32 v93, v2
	v_mov_b32_e32 v98, v2
	v_mov_b32_e32 v99, v2
	v_mov_b32_e32 v100, v2
	v_mov_b32_e32 v101, v2
	v_mov_b32_e32 v106, v2
	v_mov_b32_e32 v107, v2
	v_mov_b32_e32 v108, v2
	v_mov_b32_e32 v109, v2
	v_mov_b32_e32 v114, v2
	v_mov_b32_e32 v115, v2
	v_mov_b32_e32 v116, v2
	v_mov_b32_e32 v117, v2
	v_mov_b32_e32 v122, v2
	v_mov_b32_e32 v123, v2
	v_mov_b32_e32 v124, v2
	v_mov_b32_e32 v125, v2
	v_mov_b32_e32 v126, v2
	v_mov_b32_e32 v127, v2
	v_mov_b32_e32 v128, v2
	v_mov_b32_e32 v129, v2
	v_mov_b32_e32 v70, v2
	v_mov_b32_e32 v71, v2
	v_mov_b32_e32 v72, v2
	v_mov_b32_e32 v73, v2
	v_mov_b32_e32 v66, v2
	v_mov_b32_e32 v67, v2
	v_mov_b32_e32 v68, v2
	v_mov_b32_e32 v69, v2
	v_mov_b32_e32 v50, v2
	v_mov_b32_e32 v51, v2
	v_mov_b32_e32 v52, v2
	v_mov_b32_e32 v53, v2
	v_mov_b32_e32 v46, v2
	v_mov_b32_e32 v47, v2
	v_mov_b32_e32 v48, v2
	v_mov_b32_e32 v49, v2
	v_mov_b32_e32 v38, v2
	v_mov_b32_e32 v39, v2
	v_mov_b32_e32 v40, v2
	v_mov_b32_e32 v41, v2
	v_mov_b32_e32 v34, v2
	v_mov_b32_e32 v35, v2
	v_mov_b32_e32 v36, v2
	v_mov_b32_e32 v37, v2
	v_mov_b32_e32 v22, v2
	v_mov_b32_e32 v23, v2
	v_mov_b32_e32 v24, v2
	v_mov_b32_e32 v25, v2
	v_mov_b32_e32 v18, v2
	v_mov_b32_e32 v19, v2
	v_mov_b32_e32 v20, v2
	v_mov_b32_e32 v21, v2
	.p2align 6

; template <class Epi, class Sched, bool ALIGN_EPI = false>
; __device__ __forceinline__ void gemm_phase(PG8_LAS unsigned char* lds, const Gemm g, const Sched& S, const Epi& E) {
;     ...
;         const char* nA = Sched::GATHER ? (const char*)g.A : (has_next ? (const char*)g.A + (size_t)nxt.pm * tstep : cA); const char* nB = has_next ? (const char*)g.Bt + nxt.boff + (size_t)nxt.pn * tstep : cB;
;         for (int t = 0; t < nt; t += 2) {
;             const bool last = (t == nt - 2);
;             const char* a1 = cA + (size_t)(t + 1) * kstep;
;             const char* a2 = last ? nA : cA + (size_t)(t + 2) * kstep; const char* b2 = last ? nB : cB + (size_t)(t + 2) * kstep;
;     ...
;         for (int a = 0; a < 2; ++a)
; #pragma unroll
;             for (int b = 0; b < 2; ++b)
; #pragma unroll
;                 for (int m = 0; m < 4; ++m)
; #pragma unroll
;                     for (int n = 0; n < 2; ++n) acc[a][b][m][n] = (f32x4){0.f, 0.f, 0.f, 0.f};
.LBB0_907:
	s_ashr_i32 s41, s40, 31
	s_lshl_b64 s[50:51], s[40:41], 18
	s_add_u32 s50, s62, s50
	s_addc_u32 s51, s63, s51
	s_and_b64 s[54:55], s[52:53], exec
	s_cselect_b32 s41, s51, s59
	s_cselect_b32 s47, s50, s58
	s_add_u32 s60, s64, s44
	s_addc_u32 s61, s65, s45
	s_ashr_i32 s43, s42, 31
	s_lshl_b64 s[54:55], s[42:43], 18
	s_add_u32 s54, s60, s54
	s_addc_u32 s55, s61, s55
	s_and_b64 s[60:61], s[52:53], exec
	s_cselect_b32 s43, s55, s57
	s_cselect_b32 s89, s54, s56
	s_add_u32 s90, s56, 0x100
	s_addc_u32 s91, s57, 0
	s_add_u32 s56, s58, 0x20080
	v_mov_b32_e32 v2, 0
	s_addc_u32 s57, s59, 0
	s_mov_b32 s92, -2
	v_mov_b32_e32 v3, v2
	v_mov_b32_e32 v4, v2
	v_mov_b32_e32 v5, v2
	v_mov_b32_e32 v6, v2
	v_mov_b32_e32 v7, v2
	v_mov_b32_e32 v8, v2
	v_mov_b32_e32 v9, v2
	v_mov_b32_e32 v10, v2
	v_mov_b32_e32 v11, v2
	v_mov_b32_e32 v12, v2
	v_mov_b32_e32 v13, v2
	v_mov_b32_e32 v14, v2
	v_mov_b32_e32 v15, v2
	v_mov_b32_e32 v16, v2
	v_mov_b32_e32 v17, v2
	v_mov_b32_e32 v26, v2
	v_mov_b32_e32 v27, v2
	v_mov_b32_e32 v28, v2
	v_mov_b32_e32 v29, v2
	v_mov_b32_e32 v30, v2
	v_mov_b32_e32 v31, v2
	v_mov_b32_e32 v32, v2
	v_mov_b32_e32 v33, v2
	v_mov_b32_e32 v42, v2
	v_mov_b32_e32 v43, v2
	v_mov_b32_e32 v44, v2
	v_mov_b32_e32 v45, v2
	v_mov_b32_e32 v54, v2
	v_mov_b32_e32 v55, v2
	v_mov_b32_e32 v56, v2
	v_mov_b32_e32 v57, v2
	v_mov_b32_e32 v58, v2
	v_mov_b32_e32 v59, v2
	v_mov_b32_e32 v60, v2
	v_mov_b32_e32 v61, v2
	v_mov_b32_e32 v62, v2
	v_mov_b32_e32 v63, v2
	v_mov_b32_e32 v64, v2
	v_mov_b32_e32 v65, v2
	v_mov_b32_e32 v78, v2
	v_mov_b32_e32 v79, v2
	v_mov_b32_e32 v80, v2
	v_mov_b32_e32 v81, v2
	v_mov_b32_e32 v86, v2
	v_mov_b32_e32 v87, v2
	v_mov_b32_e32 v88, v2
	v_mov_b32_e32 v89, v2
	v_mov_b32_e32 v94, v2
	v_mov_b32_e32 v95, v2
	v_mov_b32_e32 v96, v2
	v_mov_b32_e32 v97, v2
	v_mov_b32_e32 v102, v2
	v_mov_b32_e32 v103, v2
	v_mov_b32_e32 v104, v2
	v_mov_b32_e32 v105, v2
	v_mov_b32_e32 v110, v2
	v_mov_b32_e32 v111, v2
	v_mov_b32_e32 v112, v2
	v_mov_b32_e32 v113, v2
	v_mov_b32_e32 v118, v2
	v_mov_b32_e32 v119, v2
	v_mov_b32_e32 v120, v2
	v_mov_b32_e32 v121, v2
	v_mov_b32_e32 v74, v2
	v_mov_b32_e32 v75, v2
	v_mov_b32_e32 v76, v2
	v_mov_b32_e32 v77, v2
	v_mov_b32_e32 v82, v2
	v_mov_b32_e32 v83, v2
	v_mov_b32_e32 v84, v2
	v_mov_b32_e32 v85, v2
	v_mov_b32_e32 v90, v2
	v_mov_b32_e32 v91, v2
	v_mov_b32_e32 v92, v2
	v_mov_b32_e32 v93, v2
	v_mov_b32_e32 v98, v2
	v_mov_b32_e32 v99, v2
	v_mov_b32_e32 v100, v2
	v_mov_b32_e32 v101, v2
	v_mov_b32_e32 v106, v2
	v_mov_b32_e32 v107, v2
	v_mov_b32_e32 v108, v2
	v_mov_b32_e32 v109, v2
	v_mov_b32_e32 v114, v2
	v_mov_b32_e32 v115, v2
	v_mov_b32_e32 v116, v2
	v_mov_b32_e32 v117, v2
	v_mov_b32_e32 v122, v2
	v_mov_b32_e32 v123, v2
	v_mov_b32_e32 v124, v2
	v_mov_b32_e32 v125, v2
	v_mov_b32_e32 v126, v2
	v_mov_b32_e32 v127, v2
	v_mov_b32_e32 v128, v2
	v_mov_b32_e32 v129, v2
	v_mov_b32_e32 v70, v2
	v_mov_b32_e32 v71, v2
	v_mov_b32_e32 v72, v2
	v_mov_b32_e32 v73, v2
	v_mov_b32_e32 v66, v2
	v_mov_b32_e32 v67, v2
	v_mov_b32_e32 v68, v2
	v_mov_b32_e32 v69, v2
	v_mov_b32_e32 v50, v2
	v_mov_b32_e32 v51, v2
	v_mov_b32_e32 v52, v2
	v_mov_b32_e32 v53, v2
	v_mov_b32_e32 v46, v2
	v_mov_b32_e32 v47, v2
	v_mov_b32_e32 v48, v2
	v_mov_b32_e32 v49, v2
	v_mov_b32_e32 v38, v2
	v_mov_b32_e32 v39, v2
	v_mov_b32_e32 v40, v2
	v_mov_b32_e32 v41, v2
	v_mov_b32_e32 v34, v2
	v_mov_b32_e32 v35, v2
	v_mov_b32_e32 v36, v2
	v_mov_b32_e32 v37, v2
	v_mov_b32_e32 v22, v2
	v_mov_b32_e32 v23, v2
	v_mov_b32_e32 v24, v2
	v_mov_b32_e32 v25, v2
	v_mov_b32_e32 v18, v2
	v_mov_b32_e32 v19, v2
	v_mov_b32_e32 v20, v2
	v_mov_b32_e32 v21, v2
	.p2align 6

; template <class Epi, class Sched, bool ALIGN_EPI = false>
; __device__ __forceinline__ void gemm_phase(PG8_LAS unsigned char* lds, const Gemm g, const Sched& S, const Epi& E) {
;     ...
;         const char* nA = Sched::GATHER ? (const char*)g.A : (has_next ? (const char*)g.A + (size_t)nxt.pm * tstep : cA); const char* nB = has_next ? (const char*)g.Bt + nxt.boff + (size_t)nxt.pn * tstep : cB;
;         for (int t = 0; t < nt; t += 2) {
;             const bool last = (t == nt - 2);
;             const char* a1 = cA + (size_t)(t + 1) * kstep;
;             const char* a2 = last ? nA : cA + (size_t)(t + 2) * kstep; const char* b2 = last ? nB : cB + (size_t)(t + 2) * kstep;
;     ...
;         for (int a = 0; a < 2; ++a)
; #pragma unroll
;             for (int b = 0; b < 2; ++b)
; #pragma unroll
;                 for (int m = 0; m < 4; ++m)
; #pragma unroll
;                     for (int n = 0; n < 2; ++n) acc[a][b][m][n] = (f32x4){0.f, 0.f, 0.f, 0.f};
.LBB0_1054:
	s_ashr_i32 s15, s14, 31
	s_lshl_b64 s[50:51], s[14:15], 20
	s_add_u32 s50, s12, s50
	s_addc_u32 s51, s13, s51
	s_and_b64 s[52:53], s[10:11], exec
	s_cselect_b32 s15, s51, s55
	s_cselect_b32 s79, s50, s54
	s_ashr_i32 s49, s48, 31
	s_lshl_b64 s[52:53], s[48:49], 20
	s_add_u32 s52, s3, s52
	s_addc_u32 s53, s35, s53
	s_and_b64 s[58:59], s[10:11], exec
	s_cselect_b32 s49, s53, s57
	s_cselect_b32 s80, s52, s56
	s_add_u32 s54, s54, 0x80080
	s_addc_u32 s55, s55, 0
	s_add_u32 s81, s56, 0x100
	v_mov_b32_e32 v2, 0
	s_addc_u32 s82, s57, 0
	s_mov_b32 s83, -2
	v_mov_b32_e32 v3, v2
	v_mov_b32_e32 v4, v2
	v_mov_b32_e32 v5, v2
	v_mov_b32_e32 v6, v2
	v_mov_b32_e32 v7, v2
	v_mov_b32_e32 v8, v2
	v_mov_b32_e32 v9, v2
	v_mov_b32_e32 v10, v2
	v_mov_b32_e32 v11, v2
	v_mov_b32_e32 v12, v2
	v_mov_b32_e32 v13, v2
	v_mov_b32_e32 v14, v2
	v_mov_b32_e32 v15, v2
	v_mov_b32_e32 v16, v2
	v_mov_b32_e32 v17, v2
	v_mov_b32_e32 v26, v2
	v_mov_b32_e32 v27, v2
	v_mov_b32_e32 v28, v2
	v_mov_b32_e32 v29, v2
	v_mov_b32_e32 v30, v2
	v_mov_b32_e32 v31, v2
	v_mov_b32_e32 v32, v2
	v_mov_b32_e32 v33, v2
	v_mov_b32_e32 v42, v2
	v_mov_b32_e32 v43, v2
	v_mov_b32_e32 v44, v2
	v_mov_b32_e32 v45, v2
	v_mov_b32_e32 v54, v2
	v_mov_b32_e32 v55, v2
	v_mov_b32_e32 v56, v2
	v_mov_b32_e32 v57, v2
	v_mov_b32_e32 v58, v2
	v_mov_b32_e32 v59, v2
	v_mov_b32_e32 v60, v2
	v_mov_b32_e32 v61, v2
	v_mov_b32_e32 v62, v2
	v_mov_b32_e32 v63, v2
	v_mov_b32_e32 v64, v2
	v_mov_b32_e32 v65, v2
	v_mov_b32_e32 v78, v2
	v_mov_b32_e32 v79, v2
	v_mov_b32_e32 v80, v2
	v_mov_b32_e32 v81, v2
	v_mov_b32_e32 v86, v2
	v_mov_b32_e32 v87, v2
	v_mov_b32_e32 v88, v2
	v_mov_b32_e32 v89, v2
	v_mov_b32_e32 v94, v2
	v_mov_b32_e32 v95, v2
	v_mov_b32_e32 v96, v2
	v_mov_b32_e32 v97, v2
	v_mov_b32_e32 v102, v2
	v_mov_b32_e32 v103, v2
	v_mov_b32_e32 v104, v2
	v_mov_b32_e32 v105, v2
	v_mov_b32_e32 v110, v2
	v_mov_b32_e32 v111, v2
	v_mov_b32_e32 v112, v2
	v_mov_b32_e32 v113, v2
	v_mov_b32_e32 v118, v2
	v_mov_b32_e32 v119, v2
	v_mov_b32_e32 v120, v2
	v_mov_b32_e32 v121, v2
	v_mov_b32_e32 v74, v2
	v_mov_b32_e32 v75, v2
	v_mov_b32_e32 v76, v2
	v_mov_b32_e32 v77, v2
	v_mov_b32_e32 v82, v2
	v_mov_b32_e32 v83, v2
	v_mov_b32_e32 v84, v2
	v_mov_b32_e32 v85, v2
	v_mov_b32_e32 v90, v2
	v_mov_b32_e32 v91, v2
	v_mov_b32_e32 v92, v2
	v_mov_b32_e32 v93, v2
	v_mov_b32_e32 v98, v2
	v_mov_b32_e32 v99, v2
	v_mov_b32_e32 v100, v2
	v_mov_b32_e32 v101, v2
	v_mov_b32_e32 v106, v2
	v_mov_b32_e32 v107, v2
	v_mov_b32_e32 v108, v2
	v_mov_b32_e32 v109, v2
	v_mov_b32_e32 v114, v2
	v_mov_b32_e32 v115, v2
	v_mov_b32_e32 v116, v2
	v_mov_b32_e32 v117, v2
	v_mov_b32_e32 v122, v2
	v_mov_b32_e32 v123, v2
	v_mov_b32_e32 v124, v2
	v_mov_b32_e32 v125, v2
	v_mov_b32_e32 v126, v2
	v_mov_b32_e32 v127, v2
	v_mov_b32_e32 v128, v2
	v_mov_b32_e32 v129, v2
	v_mov_b32_e32 v66, v2
	v_mov_b32_e32 v67, v2
	v_mov_b32_e32 v68, v2
	v_mov_b32_e32 v69, v2
	v_mov_b32_e32 v70, v2
	v_mov_b32_e32 v71, v2
	v_mov_b32_e32 v72, v2
	v_mov_b32_e32 v73, v2
	v_mov_b32_e32 v46, v2
	v_mov_b32_e32 v47, v2
	v_mov_b32_e32 v48, v2
	v_mov_b32_e32 v49, v2
	v_mov_b32_e32 v50, v2
	v_mov_b32_e32 v51, v2
	v_mov_b32_e32 v52, v2
	v_mov_b32_e32 v53, v2
	v_mov_b32_e32 v34, v2
	v_mov_b32_e32 v35, v2
	v_mov_b32_e32 v36, v2
	v_mov_b32_e32 v37, v2
	v_mov_b32_e32 v38, v2
	v_mov_b32_e32 v39, v2
	v_mov_b32_e32 v40, v2
	v_mov_b32_e32 v41, v2
	v_mov_b32_e32 v18, v2
	v_mov_b32_e32 v19, v2
	v_mov_b32_e32 v20, v2
	v_mov_b32_e32 v21, v2
	v_mov_b32_e32 v22, v2
	v_mov_b32_e32 v23, v2
	v_mov_b32_e32 v24, v2
	v_mov_b32_e32 v25, v2
	.p2align 6

; template <class Epi, class Sched, bool ALIGN_EPI = false>
; __device__ __forceinline__ void gemm_phase(PG8_LAS unsigned char* lds, const Gemm g, const Sched& S, const Epi& E) {
;     ...
;         const char* nA = Sched::GATHER ? (const char*)g.A : (has_next ? (const char*)g.A + (size_t)nxt.pm * tstep : cA); const char* nB = has_next ? (const char*)g.Bt + nxt.boff + (size_t)nxt.pn * tstep : cB;
;         for (int t = 0; t < nt; t += 2) {
;             const bool last = (t == nt - 2);
;             const char* a1 = cA + (size_t)(t + 1) * kstep;
;             const char* a2 = last ? nA : cA + (size_t)(t + 2) * kstep; const char* b2 = last ? nB : cB + (size_t)(t + 2) * kstep;
;     ...
;         for (int a = 0; a < 2; ++a)
; #pragma unroll
;             for (int b = 0; b < 2; ++b)
; #pragma unroll
;                 for (int m = 0; m < 4; ++m)
; #pragma unroll
;                     for (int n = 0; n < 2; ++n) acc[a][b][m][n] = (f32x4){0.f, 0.f, 0.f, 0.f};
.LBB0_1197:
	s_ashr_i32 s45, s44, 31
	s_lshl_b64 s[46:47], s[44:45], 20
	s_add_u32 s46, s3, s46
	s_addc_u32 s47, s35, s47
	s_and_b64 s[48:49], s[10:11], exec
	s_cselect_b32 s45, s47, s53
	s_cselect_b32 s74, s46, s52
	s_ashr_i32 s43, s42, 31
	s_lshl_b64 s[48:49], s[42:43], 20
	s_add_u32 s48, s58, s48
	s_addc_u32 s49, s59, s49
	s_and_b64 s[56:57], s[10:11], exec
	s_cselect_b32 s43, s49, s55
	s_cselect_b32 s75, s48, s54
	s_add_u32 s52, s52, 0x80080
	s_addc_u32 s53, s53, 0
	s_add_u32 s76, s54, 0x100
	v_mov_b32_e32 v2, 0
	s_addc_u32 s77, s55, 0
	s_mov_b32 s78, -2
	v_mov_b32_e32 v3, v2
	v_mov_b32_e32 v4, v2
	v_mov_b32_e32 v5, v2
	v_mov_b32_e32 v6, v2
	v_mov_b32_e32 v7, v2
	v_mov_b32_e32 v8, v2
	v_mov_b32_e32 v9, v2
	v_mov_b32_e32 v18, v2
	v_mov_b32_e32 v19, v2
	v_mov_b32_e32 v20, v2
	v_mov_b32_e32 v21, v2
	v_mov_b32_e32 v22, v2
	v_mov_b32_e32 v23, v2
	v_mov_b32_e32 v24, v2
	v_mov_b32_e32 v25, v2
	v_mov_b32_e32 v34, v2
	v_mov_b32_e32 v35, v2
	v_mov_b32_e32 v36, v2
	v_mov_b32_e32 v37, v2
	v_mov_b32_e32 v38, v2
	v_mov_b32_e32 v39, v2
	v_mov_b32_e32 v40, v2
	v_mov_b32_e32 v41, v2
	v_mov_b32_e32 v50, v2
	v_mov_b32_e32 v51, v2
	v_mov_b32_e32 v52, v2
	v_mov_b32_e32 v53, v2
	v_mov_b32_e32 v54, v2
	v_mov_b32_e32 v55, v2
	v_mov_b32_e32 v56, v2
	v_mov_b32_e32 v57, v2
	v_mov_b32_e32 v66, v2
	v_mov_b32_e32 v67, v2
	v_mov_b32_e32 v68, v2
	v_mov_b32_e32 v69, v2
	v_mov_b32_e32 v70, v2
	v_mov_b32_e32 v71, v2
	v_mov_b32_e32 v72, v2
	v_mov_b32_e32 v73, v2
	v_mov_b32_e32 v82, v2
	v_mov_b32_e32 v83, v2
	v_mov_b32_e32 v84, v2
	v_mov_b32_e32 v85, v2
	v_mov_b32_e32 v86, v2
	v_mov_b32_e32 v87, v2
	v_mov_b32_e32 v88, v2
	v_mov_b32_e32 v89, v2
	v_mov_b32_e32 v98, v2
	v_mov_b32_e32 v99, v2
	v_mov_b32_e32 v100, v2
	v_mov_b32_e32 v101, v2
	v_mov_b32_e32 v102, v2
	v_mov_b32_e32 v103, v2
	v_mov_b32_e32 v104, v2
	v_mov_b32_e32 v105, v2
	v_mov_b32_e32 v106, v2
	v_mov_b32_e32 v107, v2
	v_mov_b32_e32 v108, v2
	v_mov_b32_e32 v109, v2
	v_mov_b32_e32 v110, v2
	v_mov_b32_e32 v111, v2
	v_mov_b32_e32 v112, v2
	v_mov_b32_e32 v113, v2
	v_mov_b32_e32 v74, v2
	v_mov_b32_e32 v75, v2
	v_mov_b32_e32 v76, v2
	v_mov_b32_e32 v77, v2
	v_mov_b32_e32 v78, v2
	v_mov_b32_e32 v79, v2
	v_mov_b32_e32 v80, v2
	v_mov_b32_e32 v81, v2
	v_mov_b32_e32 v90, v2
	v_mov_b32_e32 v91, v2
	v_mov_b32_e32 v92, v2
	v_mov_b32_e32 v93, v2
	v_mov_b32_e32 v94, v2
	v_mov_b32_e32 v95, v2
	v_mov_b32_e32 v96, v2
	v_mov_b32_e32 v97, v2
	v_mov_b32_e32 v114, v2
	v_mov_b32_e32 v115, v2
	v_mov_b32_e32 v116, v2
	v_mov_b32_e32 v117, v2
	v_mov_b32_e32 v118, v2
	v_mov_b32_e32 v119, v2
	v_mov_b32_e32 v120, v2
	v_mov_b32_e32 v121, v2
	v_mov_b32_e32 v122, v2
	v_mov_b32_e32 v123, v2
	v_mov_b32_e32 v124, v2
	v_mov_b32_e32 v125, v2
	v_mov_b32_e32 v126, v2
	v_mov_b32_e32 v127, v2
	v_mov_b32_e32 v128, v2
	v_mov_b32_e32 v129, v2
	v_mov_b32_e32 v62, v2
	v_mov_b32_e32 v63, v2
	v_mov_b32_e32 v64, v2
	v_mov_b32_e32 v65, v2
	v_mov_b32_e32 v58, v2
	v_mov_b32_e32 v59, v2
	v_mov_b32_e32 v60, v2
	v_mov_b32_e32 v61, v2
	v_mov_b32_e32 v46, v2
	v_mov_b32_e32 v47, v2
	v_mov_b32_e32 v48, v2
	v_mov_b32_e32 v49, v2
	v_mov_b32_e32 v42, v2
	v_mov_b32_e32 v43, v2
	v_mov_b32_e32 v44, v2
	v_mov_b32_e32 v45, v2
	v_mov_b32_e32 v30, v2
	v_mov_b32_e32 v31, v2
	v_mov_b32_e32 v32, v2
	v_mov_b32_e32 v33, v2
	v_mov_b32_e32 v26, v2
	v_mov_b32_e32 v27, v2
	v_mov_b32_e32 v28, v2
	v_mov_b32_e32 v29, v2
	v_mov_b32_e32 v14, v2
	v_mov_b32_e32 v15, v2
	v_mov_b32_e32 v16, v2
	v_mov_b32_e32 v17, v2
	v_mov_b32_e32 v10, v2
	v_mov_b32_e32 v11, v2
	v_mov_b32_e32 v12, v2
	v_mov_b32_e32 v13, v2
	.p2align 6

;     __device__ __forceinline__ int arow(const Unit& u, int r) const { if (!GATHER_) return u.pm * BM + r; int slot = u.s0 + r; slot = slot < u.cnt ? slot : u.cnt - 1; return list[u.e * 16384 + slot] >> 1; }
; #define PG8_STAGE(bufoff, gbase, voff) do { _Pragma("unroll") for (int _i = 0; _i < 2; ++_i) \
;         __builtin_amdgcn_global_load_lds((const unsigned*)((const char*)(gbase) + (voff)[_i]), (PG8_LAS unsigned*)(lds + (bufoff) + ldsw + _i * 8192), 16, 0, 0); } while (0)
; template <class Epi, class Sched, bool ALIGN_EPI = false>
; __device__ __forceinline__ void gemm_phase(PG8_LAS unsigned char* lds, const Gemm g, const Sched& S, const Epi& E) {
;     ...
;     f32x4 acc[2][2][4][2];
; #pragma unroll
;     for (int a = 0; a < 2; ++a)
; #pragma unroll
;         for (int b = 0; b < 2; ++b)
; #pragma unroll
;             for (int m = 0; m < 4; ++m)
; #pragma unroll
;                 for (int n = 0; n < 2; ++n) acc[a][b][m][n] = (f32x4){0.f, 0.f, 0.f, 0.f};
;     bf16x8 At[4][2], B0[2][2], B1[2][2];
;     unsigned vc0[2], vc1[2], vn0[2], vn1[2];
;     if constexpr (Sched::GATHER) {
; #pragma unroll
;         for (int i = 0; i < 2; ++i) { vc0[i] = (unsigned)(S.arow(cur, RA[i]) * K + CA[i]) * 2u; vc1[i] = (unsigned)(S.arow(cur, RA[i] + HALF) * K + CA[i]) * 2u; vn0[i] = vc0[i]; vn1[i] = vc1[i]; }
;     } else {
; #pragma unroll
;         for (int i = 0; i < 2; ++i) { vc0[i] = voffA[i]; vc1[i] = voffA[i]; vn0[i] = voffA[i]; vn1[i] = voffA[i]; }
;     }
;     const char* cA = Sched::GATHER ? (const char*)g.A : (const char*)g.A + (size_t)cur.pm * tstep; const char* cB = (const char*)g.Bt + cur.boff + (size_t)cur.pn * tstep;
;     S.a_ready(cur);
;     PG8_STAGE(PG8_SB(0, 0), cB, voffB); PG8_STAGE(PG8_SB(0, 1), cB + hstep, voffB); PG8_STAGE(PG8_SA(0, 0), cA, vc0); PG8_STAGE(PG8_SA(0, 1), cA + hstepA, vc1);
.LBB0_1413:
	v_mov_b32_e32 v153, v135
	v_mov_b32_e32 v155, v135
	s_add_u32 s47, s54, 0x100
	v_mov_b32_e32 v26, 0
	s_addc_u32 s86, s55, 0
	v_lshl_add_u64 v[158:159], s[26:27], 0, v[154:155]
	v_lshl_add_u64 v[160:161], s[26:27], 0, v[152:153]
	s_mov_b32 s87, -2
	s_mov_b64 s[54:55], 0
	v_mov_b32_e32 v27, v26
	v_mov_b32_e32 v28, v26
	v_mov_b32_e32 v29, v26
	v_mov_b32_e32 v38, v26
	v_mov_b32_e32 v39, v26
	v_mov_b32_e32 v40, v26
	v_mov_b32_e32 v41, v26
	v_mov_b32_e32 v46, v26
	v_mov_b32_e32 v47, v26
	v_mov_b32_e32 v48, v26
	v_mov_b32_e32 v49, v26
	v_mov_b32_e32 v54, v26
	v_mov_b32_e32 v55, v26
	v_mov_b32_e32 v56, v26
	v_mov_b32_e32 v57, v26
	v_mov_b32_e32 v2, v26
	v_mov_b32_e32 v3, v26
	v_mov_b32_e32 v4, v26
	v_mov_b32_e32 v5, v26
	v_mov_b32_e32 v14, v26
	v_mov_b32_e32 v15, v26
	v_mov_b32_e32 v16, v26
	v_mov_b32_e32 v17, v26
	v_mov_b32_e32 v30, v26
	v_mov_b32_e32 v31, v26
	v_mov_b32_e32 v32, v26
	v_mov_b32_e32 v33, v26
	v_mov_b32_e32 v34, v26
	v_mov_b32_e32 v35, v26
	v_mov_b32_e32 v36, v26
	v_mov_b32_e32 v37, v26
	v_mov_b32_e32 v42, v26
	v_mov_b32_e32 v43, v26
	v_mov_b32_e32 v44, v26
	v_mov_b32_e32 v45, v26
	v_mov_b32_e32 v50, v26
	v_mov_b32_e32 v51, v26
	v_mov_b32_e32 v52, v26
	v_mov_b32_e32 v53, v26
	v_mov_b32_e32 v58, v26
	v_mov_b32_e32 v59, v26
	v_mov_b32_e32 v60, v26
	v_mov_b32_e32 v61, v26
	v_mov_b32_e32 v62, v26
	v_mov_b32_e32 v63, v26
	v_mov_b32_e32 v64, v26
	v_mov_b32_e32 v65, v26
	v_mov_b32_e32 v66, v26
	v_mov_b32_e32 v67, v26
	v_mov_b32_e32 v68, v26
	v_mov_b32_e32 v69, v26
	v_mov_b32_e32 v70, v26
	v_mov_b32_e32 v71, v26
	v_mov_b32_e32 v72, v26
	v_mov_b32_e32 v73, v26
	v_mov_b32_e32 v82, v26
	v_mov_b32_e32 v83, v26
	v_mov_b32_e32 v84, v26
	v_mov_b32_e32 v85, v26
	v_mov_b32_e32 v86, v26
	v_mov_b32_e32 v87, v26
	v_mov_b32_e32 v88, v26
	v_mov_b32_e32 v89, v26
	v_mov_b32_e32 v98, v26
	v_mov_b32_e32 v99, v26
	v_mov_b32_e32 v100, v26
	v_mov_b32_e32 v101, v26
	v_mov_b32_e32 v102, v26
	v_mov_b32_e32 v103, v26
	v_mov_b32_e32 v104, v26
	v_mov_b32_e32 v105, v26
	v_mov_b32_e32 v114, v26
	v_mov_b32_e32 v115, v26
	v_mov_b32_e32 v116, v26
	v_mov_b32_e32 v117, v26
	v_mov_b32_e32 v118, v26
	v_mov_b32_e32 v119, v26
	v_mov_b32_e32 v120, v26
	v_mov_b32_e32 v121, v26
	v_mov_b32_e32 v74, v26
	v_mov_b32_e32 v75, v26
	v_mov_b32_e32 v76, v26
	v_mov_b32_e32 v77, v26
	v_mov_b32_e32 v78, v26
	v_mov_b32_e32 v79, v26
	v_mov_b32_e32 v80, v26
	v_mov_b32_e32 v81, v26
	v_mov_b32_e32 v90, v26
	v_mov_b32_e32 v91, v26
	v_mov_b32_e32 v92, v26
	v_mov_b32_e32 v93, v26
	v_mov_b32_e32 v94, v26
	v_mov_b32_e32 v95, v26
	v_mov_b32_e32 v96, v26
	v_mov_b32_e32 v97, v26
	v_mov_b32_e32 v106, v26
	v_mov_b32_e32 v107, v26
	v_mov_b32_e32 v108, v26
	v_mov_b32_e32 v109, v26
	v_mov_b32_e32 v110, v26
	v_mov_b32_e32 v111, v26
	v_mov_b32_e32 v112, v26
	v_mov_b32_e32 v113, v26
	v_mov_b32_e32 v122, v26
	v_mov_b32_e32 v123, v26
	v_mov_b32_e32 v124, v26
	v_mov_b32_e32 v125, v26
	v_mov_b32_e32 v126, v26
	v_mov_b32_e32 v127, v26
	v_mov_b32_e32 v128, v26
	v_mov_b32_e32 v129, v26
	v_mov_b32_e32 v22, v26
	v_mov_b32_e32 v23, v26
	v_mov_b32_e32 v24, v26
	v_mov_b32_e32 v25, v26
	v_mov_b32_e32 v18, v26
	v_mov_b32_e32 v19, v26
	v_mov_b32_e32 v20, v26
	v_mov_b32_e32 v21, v26
	v_mov_b32_e32 v10, v26
	v_mov_b32_e32 v11, v26
	v_mov_b32_e32 v12, v26
	v_mov_b32_e32 v13, v26
	v_mov_b32_e32 v6, v26
	v_mov_b32_e32 v7, v26
	v_mov_b32_e32 v8, v26
	v_mov_b32_e32 v9, v26
	.p2align 6

; #define PG8_STAGE(bufoff, gbase, voff) do { _Pragma("unroll") for (int _i = 0; _i < 2; ++_i) \
;         __builtin_amdgcn_global_load_lds((const unsigned*)((const char*)(gbase) + (voff)[_i]), (PG8_LAS unsigned*)(lds + (bufoff) + ldsw + _i * 8192), 16, 0, 0); } while (0)
; #define PG8_WAIT_V(n) asm volatile("s_waitcnt vmcnt(" #n ")" ::: "memory")
; #define PG8_BAR __builtin_amdgcn_s_barrier()
;     __device__ __forceinline__ Pre pre(const Unit& u, int wr, int fr) const { Pre p; const int rl0 = wr * 64 + fr;
; #pragma unroll
;         for (int ai = 0; ai < 2; ++ai)
; #pragma unroll
;             for (int m = 0; m < 4; ++m) { int slot = u.s0 + rl0 + ai * HALF + m * 16; slot = slot < u.cnt ? slot : u.cnt - 1; p.rs[ai][m] = lrs[u.e * 16384 + slot]; }
;         return p; }
; template <class Epi, class Sched, bool ALIGN_EPI = false>
; __device__ __forceinline__ void gemm_phase(PG8_LAS unsigned char* lds, const Gemm g, const Sched& S, const Epi& E) {
;     ...
;     PG8_STAGE(PG8_SB(0, 0), cB, voffB); PG8_STAGE(PG8_SB(0, 1), cB + hstep, voffB); PG8_STAGE(PG8_SA(0, 0), cA, vc0); PG8_STAGE(PG8_SA(0, 1), cA + hstepA, vc1);
;     if (wr == 1) PG8_BAR;
;     PG8_WAIT_V(2); PG8_BAR;
;     PG8_STAGE(PG8_SB(1, 0), cB + kstep, voffB); PG8_STAGE(PG8_SA(1, 0), cA + kstep, vc0); PG8_STAGE(PG8_SB(1, 1), cB + hstep + kstep, voffB);
;     PG8_WAIT_V(6); PG8_BAR;
;     for (;;) {
;         typename Epi::Pre pf;
;         if constexpr (Epi::KSCALE) pf = E.pre2(cur, lds, ui, tid); else pf = E.pre(cur, wr, fr);
;         const bool has_next = S.next(ui + 1, nxt);
.LBB0_1479:
	s_add_u32 s18, s36, 0x30800000
	v_lshlrev_b32_e32 v9, 2, v162
	s_addc_u32 s19, s37, 0
	v_lshl_or_b32 v166, s13, 6, v162
	v_lshl_or_b32 v8, v162, 6, v163
	s_lshl_b32 s13, s13, 13
	v_and_b32_e32 v9, 32, v9
	s_lshl_b32 s12, s12, 5
	v_bitop3_b32 v20, v8, s13, v9 bitop3:0xde
	s_and_b32 s40, s12, 0x60
	s_mov_b64 s[12:13], 0x80
	s_add_i32 m0, s25, 0x18000
	v_lshl_add_u64 v[4:5], v[4:5], 0, s[12:13]
	s_waitcnt vmcnt(2)
	s_barrier
	global_load_lds_dwordx4 v[4:5], off
	s_add_i32 m0, s25, 0x1a000
	s_add_u32 s48, s36, 0x3c800080
	v_lshl_add_u64 v[2:3], v[2:3], 0, s[12:13]
	s_addc_u32 s49, s37, 0
	s_add_i32 s41, s25, 0x8000
	global_load_lds_dwordx4 v[2:3], off
	v_lshl_add_u64 v[2:3], s[48:49], 0, v[148:149]
	s_mov_b32 m0, s41
	s_add_i32 s42, s25, 0xa000
	global_load_lds_dwordx4 v[2:3], off
	v_lshl_add_u64 v[2:3], s[48:49], 0, v[150:151]
	s_add_u32 s48, s10, 0x80080
	s_mov_b32 m0, s42
	s_addc_u32 s49, s11, 0
	global_load_lds_dwordx4 v[2:3], off
	s_add_i32 m0, s25, 0x1c000
	v_lshl_add_u64 v[2:3], s[48:49], 0, v[146:147]
	global_load_lds_dwordx4 v[2:3], off
	v_lshl_add_u64 v[2:3], s[48:49], 0, v[144:145]
	s_add_i32 m0, s25, 0x1e000
	v_add_u32_e32 v18, s46, v166
	global_load_lds_dwordx4 v[2:3], off
	v_min_i32_e32 v2, s44, v18
	v_add_u32_e32 v4, 16, v18
	v_add_u32_e32 v8, 32, v18
	v_add_u32_e32 v10, 48, v18
	v_add_u32_e32 v12, 0x80, v18
	v_add_u32_e32 v14, 0x90, v18
	v_add_u32_e32 v16, 0xa0, v18
	v_add_u32_e32 v18, 0xb0, v18
	v_add_u32_e32 v2, s43, v2
	v_min_i32_e32 v4, s44, v4
	v_min_i32_e32 v8, s44, v8
	v_min_i32_e32 v10, s44, v10
	v_min_i32_e32 v12, s44, v12
	v_min_i32_e32 v14, s44, v14
	v_min_i32_e32 v16, s44, v16
	v_min_i32_e32 v18, s44, v18
	v_ashrrev_i32_e32 v3, 31, v2
	v_add_u32_e32 v4, s43, v4
	v_add_u32_e32 v8, s43, v8
	v_add_u32_e32 v10, s43, v10
	v_add_u32_e32 v12, s43, v12
	v_add_u32_e32 v14, s43, v14
	v_add_u32_e32 v16, s43, v16
	v_add_u32_e32 v18, s43, v18
	v_lshl_add_u64 v[2:3], v[2:3], 2, s[18:19]
	v_ashrrev_i32_e32 v5, 31, v4
	v_ashrrev_i32_e32 v9, 31, v8
	v_ashrrev_i32_e32 v11, 31, v10
	v_ashrrev_i32_e32 v13, 31, v12
	v_ashrrev_i32_e32 v15, 31, v14
	v_ashrrev_i32_e32 v17, 31, v16
	v_ashrrev_i32_e32 v19, 31, v18
	s_waitcnt vmcnt(6)
	s_barrier
	v_lshl_add_u64 v[4:5], v[4:5], 2, s[18:19]
	v_lshl_add_u64 v[8:9], v[8:9], 2, s[18:19]
	v_lshl_add_u64 v[10:11], v[10:11], 2, s[18:19]
	v_lshl_add_u64 v[12:13], v[12:13], 2, s[18:19]
	v_lshl_add_u64 v[14:15], v[14:15], 2, s[18:19]
	v_lshl_add_u64 v[16:17], v[16:17], 2, s[18:19]
	v_lshl_add_u64 v[18:19], v[18:19], 2, s[18:19]
	global_load_dword v156, v[2:3], off
	global_load_dword v142, v[4:5], off
	global_load_dword v140, v[8:9], off
	global_load_dword v138, v[10:11], off
	global_load_dword v136, v[12:13], off
	global_load_dword v134, v[14:15], off
	global_load_dword v132, v[16:17], off
	global_load_dword v130, v[18:19], off
	s_add_u32 s14, s14, s45
	s_addc_u32 s15, s15, 0
	s_add_u32 s43, s14, 0xc800100
	v_lshl_or_b32 v21, s40, 7, v164
	s_mov_b64 s[16:17], 0x3c800080
	s_addc_u32 s44, s15, 0
	v_add3_u32 v2, v1, v7, v141
	v_mov_b32_e32 v3, v147
	s_add_i32 s48, 0, 0x10000
	s_add_i32 s50, 0, 0x14000
	s_add_i32 s52, 0, 0x18000
	s_add_i32 s14, 0, 0x1c000
	v_lshl_add_u64 v[158:159], v[2:3], 0, s[16:17]
	v_add3_u32 v2, v1, v6, v141
	v_add_u32_e32 v167, s48, v21
	v_add_u32_e32 v168, s50, v21
	s_add_i32 s48, s48, s54
	s_add_i32 s50, s50, s54
	v_add_u32_e32 v170, s52, v21
	s_add_i32 s52, s52, s54
	s_add_i32 s54, s14, s54
	v_mov_b32_e32 v153, v147
	v_mov_b32_e32 v155, v147
	v_lshl_add_u64 v[160:161], v[2:3], 0, s[16:17]
	s_mov_b32 s45, -2
	v_add_u32_e32 v169, 0, v20
	s_add_i32 s46, s25, 0xc000
	s_add_i32 s47, s25, 0xe000
	s_add_i32 s49, s48, 0x2000
	s_add_i32 s51, s50, 0x2000
	v_add_u32_e32 v171, s14, v21
	s_add_i32 s53, s52, 0x2000
	s_add_i32 s55, s54, 0x2000
	s_mov_b64 s[14:15], s[36:37]
	v_mov_b32_e32 v30, v147
	v_mov_b32_e32 v31, v147
	v_mov_b32_e32 v32, v147
	v_mov_b32_e32 v33, v147
	v_mov_b32_e32 v38, v147
	v_mov_b32_e32 v39, v147
	v_mov_b32_e32 v40, v147
	v_mov_b32_e32 v41, v147
	v_mov_b32_e32 v46, v147
	v_mov_b32_e32 v47, v147
	v_mov_b32_e32 v48, v147
	v_mov_b32_e32 v49, v147
	v_mov_b32_e32 v54, v147
	v_mov_b32_e32 v55, v147
	v_mov_b32_e32 v56, v147
	v_mov_b32_e32 v57, v147
	v_mov_b32_e32 v2, v147
	v_mov_b32_e32 v4, v147
	v_mov_b32_e32 v5, v147
	v_mov_b32_e32 v14, v147
	v_mov_b32_e32 v15, v147
	v_mov_b32_e32 v16, v147
	v_mov_b32_e32 v17, v147
	v_mov_b32_e32 v26, v147
	v_mov_b32_e32 v27, v147
	v_mov_b32_e32 v28, v147
	v_mov_b32_e32 v29, v147
	v_mov_b32_e32 v34, v147
	v_mov_b32_e32 v35, v147
	v_mov_b32_e32 v36, v147
	v_mov_b32_e32 v37, v147
	v_mov_b32_e32 v42, v147
	v_mov_b32_e32 v43, v147
	v_mov_b32_e32 v44, v147
	v_mov_b32_e32 v45, v147
	v_mov_b32_e32 v50, v147
	v_mov_b32_e32 v51, v147
	v_mov_b32_e32 v52, v147
	v_mov_b32_e32 v53, v147
	v_mov_b32_e32 v58, v147
	v_mov_b32_e32 v59, v147
	v_mov_b32_e32 v60, v147
	v_mov_b32_e32 v61, v147
	v_mov_b32_e32 v62, v147
	v_mov_b32_e32 v63, v147
	v_mov_b32_e32 v64, v147
	v_mov_b32_e32 v65, v147
	v_mov_b32_e32 v66, v147
	v_mov_b32_e32 v67, v147
	v_mov_b32_e32 v68, v147
	v_mov_b32_e32 v69, v147
	v_mov_b32_e32 v70, v147
	v_mov_b32_e32 v71, v147
	v_mov_b32_e32 v72, v147
	v_mov_b32_e32 v73, v147
	v_mov_b32_e32 v82, v147
	v_mov_b32_e32 v83, v147
	v_mov_b32_e32 v84, v147
	v_mov_b32_e32 v85, v147
	v_mov_b32_e32 v86, v147
	v_mov_b32_e32 v87, v147
	v_mov_b32_e32 v88, v147
	v_mov_b32_e32 v89, v147
	v_mov_b32_e32 v98, v147
	v_mov_b32_e32 v99, v147
	v_mov_b32_e32 v100, v147
	v_mov_b32_e32 v101, v147
	v_mov_b32_e32 v102, v147
	v_mov_b32_e32 v103, v147
	v_mov_b32_e32 v104, v147
	v_mov_b32_e32 v105, v147
	v_mov_b32_e32 v114, v147
	v_mov_b32_e32 v115, v147
	v_mov_b32_e32 v116, v147
	v_mov_b32_e32 v117, v147
	v_mov_b32_e32 v118, v147
	v_mov_b32_e32 v119, v147
	v_mov_b32_e32 v120, v147
	v_mov_b32_e32 v121, v147
	v_mov_b32_e32 v74, v147
	v_mov_b32_e32 v75, v147
	v_mov_b32_e32 v76, v147
	v_mov_b32_e32 v77, v147
	v_mov_b32_e32 v78, v147
	v_mov_b32_e32 v79, v147
	v_mov_b32_e32 v80, v147
	v_mov_b32_e32 v81, v147
	v_mov_b32_e32 v90, v147
	v_mov_b32_e32 v91, v147
	v_mov_b32_e32 v92, v147
	v_mov_b32_e32 v93, v147
	v_mov_b32_e32 v94, v147
	v_mov_b32_e32 v95, v147
	v_mov_b32_e32 v96, v147
	v_mov_b32_e32 v97, v147
	v_mov_b32_e32 v106, v147
	v_mov_b32_e32 v107, v147
	v_mov_b32_e32 v108, v147
	v_mov_b32_e32 v109, v147
	v_mov_b32_e32 v110, v147
	v_mov_b32_e32 v111, v147
	v_mov_b32_e32 v112, v147
	v_mov_b32_e32 v113, v147
	v_mov_b32_e32 v122, v147
	v_mov_b32_e32 v123, v147
	v_mov_b32_e32 v124, v147
	v_mov_b32_e32 v125, v147
	v_mov_b32_e32 v126, v147
	v_mov_b32_e32 v127, v147
	v_mov_b32_e32 v128, v147
	v_mov_b32_e32 v129, v147
	v_mov_b32_e32 v22, v147
	v_mov_b32_e32 v23, v147
	v_mov_b32_e32 v24, v147
	v_mov_b32_e32 v25, v147
	v_mov_b32_e32 v18, v147
	v_mov_b32_e32 v19, v147
	v_mov_b32_e32 v20, v147
	v_mov_b32_e32 v21, v147
	v_mov_b32_e32 v10, v147
	v_mov_b32_e32 v11, v147
	v_mov_b32_e32 v12, v147
	v_mov_b32_e32 v13, v147
	v_mov_b32_e32 v6, v147
	v_mov_b32_e32 v7, v147
	v_mov_b32_e32 v8, v147
	v_mov_b32_e32 v9, v147
	.p2align 6

; template <class Epi, class Sched, bool ALIGN_EPI = false>
; __device__ __forceinline__ void gemm_phase(PG8_LAS unsigned char* lds, const Gemm g, const Sched& S, const Epi& E) {
;     ...
;         const char* nA = Sched::GATHER ? (const char*)g.A : (has_next ? (const char*)g.A + (size_t)nxt.pm * tstep : cA); const char* nB = has_next ? (const char*)g.Bt + nxt.boff + (size_t)nxt.pn * tstep : cB;
;         for (int t = 0; t < nt; t += 2) {
;             const bool last = (t == nt - 2);
;             const char* a1 = cA + (size_t)(t + 1) * kstep;
;             const char* a2 = last ? nA : cA + (size_t)(t + 2) * kstep; const char* b2 = last ? nB : cB + (size_t)(t + 2) * kstep;
;     ...
;         for (int a = 0; a < 2; ++a)
; #pragma unroll
;             for (int b = 0; b < 2; ++b)
; #pragma unroll
;                 for (int m = 0; m < 4; ++m)
; #pragma unroll
;                     for (int n = 0; n < 2; ++n) acc[a][b][m][n] = (f32x4){0.f, 0.f, 0.f, 0.f};
.LBB0_1497:
	s_ashr_i32 s41, s40, 31
	s_lshl_b64 s[48:49], s[40:41], 18
	s_add_u32 s48, s8, s48
	s_addc_u32 s49, s9, s49
	s_and_b64 s[50:51], s[46:47], exec
	s_cselect_b32 s41, s49, s59
	s_cselect_b32 s53, s48, s58
	s_add_u32 s60, s3, s44
	s_addc_u32 s61, s35, s45
	s_ashr_i32 s43, s42, 31
	s_lshl_b64 s[50:51], s[42:43], 18
	s_add_u32 s50, s60, s50
	s_addc_u32 s51, s61, s51
	s_and_b64 s[60:61], s[46:47], exec
	s_cselect_b32 s43, s51, s57
	s_cselect_b32 s84, s50, s56
	s_add_u32 s85, s56, 0x100
	s_addc_u32 s86, s57, 0
	s_add_u32 s56, s58, 0x20080
	v_mov_b32_e32 v2, 0
	s_addc_u32 s57, s59, 0
	s_mov_b32 s87, -2
	v_mov_b32_e32 v3, v2
	v_mov_b32_e32 v4, v2
	v_mov_b32_e32 v5, v2
	v_mov_b32_e32 v6, v2
	v_mov_b32_e32 v7, v2
	v_mov_b32_e32 v8, v2
	v_mov_b32_e32 v9, v2
	v_mov_b32_e32 v10, v2
	v_mov_b32_e32 v11, v2
	v_mov_b32_e32 v12, v2
	v_mov_b32_e32 v13, v2
	v_mov_b32_e32 v14, v2
	v_mov_b32_e32 v15, v2
	v_mov_b32_e32 v16, v2
	v_mov_b32_e32 v17, v2
	v_mov_b32_e32 v26, v2
	v_mov_b32_e32 v27, v2
	v_mov_b32_e32 v28, v2
	v_mov_b32_e32 v29, v2
	v_mov_b32_e32 v30, v2
	v_mov_b32_e32 v31, v2
	v_mov_b32_e32 v32, v2
	v_mov_b32_e32 v33, v2
	v_mov_b32_e32 v42, v2
	v_mov_b32_e32 v43, v2
	v_mov_b32_e32 v44, v2
	v_mov_b32_e32 v45, v2
	v_mov_b32_e32 v54, v2
	v_mov_b32_e32 v55, v2
	v_mov_b32_e32 v56, v2
	v_mov_b32_e32 v57, v2
	v_mov_b32_e32 v58, v2
	v_mov_b32_e32 v59, v2
	v_mov_b32_e32 v60, v2
	v_mov_b32_e32 v61, v2
	v_mov_b32_e32 v62, v2
	v_mov_b32_e32 v63, v2
	v_mov_b32_e32 v64, v2
	v_mov_b32_e32 v65, v2
	v_mov_b32_e32 v78, v2
	v_mov_b32_e32 v79, v2
	v_mov_b32_e32 v80, v2
	v_mov_b32_e32 v81, v2
	v_mov_b32_e32 v86, v2
	v_mov_b32_e32 v87, v2
	v_mov_b32_e32 v88, v2
	v_mov_b32_e32 v89, v2
	v_mov_b32_e32 v94, v2
	v_mov_b32_e32 v95, v2
	v_mov_b32_e32 v96, v2
	v_mov_b32_e32 v97, v2
	v_mov_b32_e32 v102, v2
	v_mov_b32_e32 v103, v2
	v_mov_b32_e32 v104, v2
	v_mov_b32_e32 v105, v2
	v_mov_b32_e32 v110, v2
	v_mov_b32_e32 v111, v2
	v_mov_b32_e32 v112, v2
	v_mov_b32_e32 v113, v2
	v_mov_b32_e32 v118, v2
	v_mov_b32_e32 v119, v2
	v_mov_b32_e32 v120, v2
	v_mov_b32_e32 v121, v2
	v_mov_b32_e32 v74, v2
	v_mov_b32_e32 v75, v2
	v_mov_b32_e32 v76, v2
	v_mov_b32_e32 v77, v2
	v_mov_b32_e32 v82, v2
	v_mov_b32_e32 v83, v2
	v_mov_b32_e32 v84, v2
	v_mov_b32_e32 v85, v2
	v_mov_b32_e32 v90, v2
	v_mov_b32_e32 v91, v2
	v_mov_b32_e32 v92, v2
	v_mov_b32_e32 v93, v2
	v_mov_b32_e32 v98, v2
	v_mov_b32_e32 v99, v2
	v_mov_b32_e32 v100, v2
	v_mov_b32_e32 v101, v2
	v_mov_b32_e32 v106, v2
	v_mov_b32_e32 v107, v2
	v_mov_b32_e32 v108, v2
	v_mov_b32_e32 v109, v2
	v_mov_b32_e32 v114, v2
	v_mov_b32_e32 v115, v2
	v_mov_b32_e32 v116, v2
	v_mov_b32_e32 v117, v2
	v_mov_b32_e32 v122, v2
	v_mov_b32_e32 v123, v2
	v_mov_b32_e32 v124, v2
	v_mov_b32_e32 v125, v2
	v_mov_b32_e32 v126, v2
	v_mov_b32_e32 v127, v2
	v_mov_b32_e32 v128, v2
	v_mov_b32_e32 v129, v2
	v_mov_b32_e32 v70, v2
	v_mov_b32_e32 v71, v2
	v_mov_b32_e32 v72, v2
	v_mov_b32_e32 v73, v2
	v_mov_b32_e32 v66, v2
	v_mov_b32_e32 v67, v2
	v_mov_b32_e32 v68, v2
	v_mov_b32_e32 v69, v2
	v_mov_b32_e32 v50, v2
	v_mov_b32_e32 v51, v2
	v_mov_b32_e32 v52, v2
	v_mov_b32_e32 v53, v2
	v_mov_b32_e32 v46, v2
	v_mov_b32_e32 v47, v2
	v_mov_b32_e32 v48, v2
	v_mov_b32_e32 v49, v2
	v_mov_b32_e32 v38, v2
	v_mov_b32_e32 v39, v2
	v_mov_b32_e32 v40, v2
	v_mov_b32_e32 v41, v2
	v_mov_b32_e32 v34, v2
	v_mov_b32_e32 v35, v2
	v_mov_b32_e32 v36, v2
	v_mov_b32_e32 v37, v2
	v_mov_b32_e32 v22, v2
	v_mov_b32_e32 v23, v2
	v_mov_b32_e32 v24, v2
	v_mov_b32_e32 v25, v2
	v_mov_b32_e32 v18, v2
	v_mov_b32_e32 v19, v2
	v_mov_b32_e32 v20, v2
	v_mov_b32_e32 v21, v2
	.p2align 6

; template <class Epi, class Sched, bool ALIGN_EPI = false>
; __device__ __forceinline__ void gemm_phase(PG8_LAS unsigned char* lds, const Gemm g, const Sched& S, const Epi& E) {
;     ...
;         const char* nA = Sched::GATHER ? (const char*)g.A : (has_next ? (const char*)g.A + (size_t)nxt.pm * tstep : cA); const char* nB = has_next ? (const char*)g.Bt + nxt.boff + (size_t)nxt.pn * tstep : cB;
;         for (int t = 0; t < nt; t += 2) {
;             const bool last = (t == nt - 2);
;             const char* a1 = cA + (size_t)(t + 1) * kstep;
;             const char* a2 = last ? nA : cA + (size_t)(t + 2) * kstep; const char* b2 = last ? nB : cB + (size_t)(t + 2) * kstep;
;     ...
;         for (int a = 0; a < 2; ++a)
; #pragma unroll
;             for (int b = 0; b < 2; ++b)
; #pragma unroll
;                 for (int m = 0; m < 4; ++m)
; #pragma unroll
;                     for (int n = 0; n < 2; ++n) acc[a][b][m][n] = (f32x4){0.f, 0.f, 0.f, 0.f};
.LBB0_1600:
	s_ashr_i32 s25, s24, 31
	s_lshl_b64 s[46:47], s[24:25], 18
	s_add_u32 s46, s58, s46
	s_addc_u32 s47, s59, s47
	s_and_b64 s[50:51], s[48:49], exec
	s_cselect_b32 s25, s47, s55
	s_cselect_b32 s43, s46, s54
	s_add_u32 s56, s60, s40
	s_addc_u32 s57, s61, s41
	s_ashr_i32 s27, s26, 31
	s_lshl_b64 s[50:51], s[26:27], 18
	s_add_u32 s50, s56, s50
	s_addc_u32 s51, s57, s51
	s_and_b64 s[56:57], s[48:49], exec
	s_cselect_b32 s27, s51, s53
	s_cselect_b32 s84, s50, s52
	s_add_u32 s85, s52, 0x100
	s_addc_u32 s86, s53, 0
	s_add_u32 s52, s54, 0x20080
	v_mov_b32_e32 v2, 0
	s_addc_u32 s53, s55, 0
	s_mov_b32 s87, -2
	v_mov_b32_e32 v3, v2
	v_mov_b32_e32 v4, v2
	v_mov_b32_e32 v5, v2
	v_mov_b32_e32 v6, v2
	v_mov_b32_e32 v7, v2
	v_mov_b32_e32 v8, v2
	v_mov_b32_e32 v9, v2
	v_mov_b32_e32 v10, v2
	v_mov_b32_e32 v11, v2
	v_mov_b32_e32 v12, v2
	v_mov_b32_e32 v13, v2
	v_mov_b32_e32 v14, v2
	v_mov_b32_e32 v15, v2
	v_mov_b32_e32 v16, v2
	v_mov_b32_e32 v17, v2
	v_mov_b32_e32 v26, v2
	v_mov_b32_e32 v27, v2
	v_mov_b32_e32 v28, v2
	v_mov_b32_e32 v29, v2
	v_mov_b32_e32 v30, v2
	v_mov_b32_e32 v31, v2
	v_mov_b32_e32 v32, v2
	v_mov_b32_e32 v33, v2
	v_mov_b32_e32 v42, v2
	v_mov_b32_e32 v43, v2
	v_mov_b32_e32 v44, v2
	v_mov_b32_e32 v45, v2
	v_mov_b32_e32 v54, v2
	v_mov_b32_e32 v55, v2
	v_mov_b32_e32 v56, v2
	v_mov_b32_e32 v57, v2
	v_mov_b32_e32 v58, v2
	v_mov_b32_e32 v59, v2
	v_mov_b32_e32 v60, v2
	v_mov_b32_e32 v61, v2
	v_mov_b32_e32 v62, v2
	v_mov_b32_e32 v63, v2
	v_mov_b32_e32 v64, v2
	v_mov_b32_e32 v65, v2
	v_mov_b32_e32 v78, v2
	v_mov_b32_e32 v79, v2
	v_mov_b32_e32 v80, v2
	v_mov_b32_e32 v81, v2
	v_mov_b32_e32 v86, v2
	v_mov_b32_e32 v87, v2
	v_mov_b32_e32 v88, v2
	v_mov_b32_e32 v89, v2
	v_mov_b32_e32 v94, v2
	v_mov_b32_e32 v95, v2
	v_mov_b32_e32 v96, v2
	v_mov_b32_e32 v97, v2
	v_mov_b32_e32 v102, v2
	v_mov_b32_e32 v103, v2
	v_mov_b32_e32 v104, v2
	v_mov_b32_e32 v105, v2
	v_mov_b32_e32 v110, v2
	v_mov_b32_e32 v111, v2
	v_mov_b32_e32 v112, v2
	v_mov_b32_e32 v113, v2
	v_mov_b32_e32 v118, v2
	v_mov_b32_e32 v119, v2
	v_mov_b32_e32 v120, v2
	v_mov_b32_e32 v121, v2
	v_mov_b32_e32 v74, v2
	v_mov_b32_e32 v75, v2
	v_mov_b32_e32 v76, v2
	v_mov_b32_e32 v77, v2
	v_mov_b32_e32 v82, v2
	v_mov_b32_e32 v83, v2
	v_mov_b32_e32 v84, v2
	v_mov_b32_e32 v85, v2
	v_mov_b32_e32 v90, v2
	v_mov_b32_e32 v91, v2
	v_mov_b32_e32 v92, v2
	v_mov_b32_e32 v93, v2
	v_mov_b32_e32 v98, v2
	v_mov_b32_e32 v99, v2
	v_mov_b32_e32 v100, v2
	v_mov_b32_e32 v101, v2
	v_mov_b32_e32 v106, v2
	v_mov_b32_e32 v107, v2
	v_mov_b32_e32 v108, v2
	v_mov_b32_e32 v109, v2
	v_mov_b32_e32 v114, v2
	v_mov_b32_e32 v115, v2
	v_mov_b32_e32 v116, v2
	v_mov_b32_e32 v117, v2
	v_mov_b32_e32 v122, v2
	v_mov_b32_e32 v123, v2
	v_mov_b32_e32 v124, v2
	v_mov_b32_e32 v125, v2
	v_mov_b32_e32 v126, v2
	v_mov_b32_e32 v127, v2
	v_mov_b32_e32 v128, v2
	v_mov_b32_e32 v129, v2
	v_mov_b32_e32 v70, v2
	v_mov_b32_e32 v71, v2
	v_mov_b32_e32 v72, v2
	v_mov_b32_e32 v73, v2
	v_mov_b32_e32 v66, v2
	v_mov_b32_e32 v67, v2
	v_mov_b32_e32 v68, v2
	v_mov_b32_e32 v69, v2
	v_mov_b32_e32 v50, v2
	v_mov_b32_e32 v51, v2
	v_mov_b32_e32 v52, v2
	v_mov_b32_e32 v53, v2
	v_mov_b32_e32 v46, v2
	v_mov_b32_e32 v47, v2
	v_mov_b32_e32 v48, v2
	v_mov_b32_e32 v49, v2
	v_mov_b32_e32 v38, v2
	v_mov_b32_e32 v39, v2
	v_mov_b32_e32 v40, v2
	v_mov_b32_e32 v41, v2
	v_mov_b32_e32 v34, v2
	v_mov_b32_e32 v35, v2
	v_mov_b32_e32 v36, v2
	v_mov_b32_e32 v37, v2
	v_mov_b32_e32 v22, v2
	v_mov_b32_e32 v23, v2
	v_mov_b32_e32 v24, v2
	v_mov_b32_e32 v25, v2
	v_mov_b32_e32 v18, v2
	v_mov_b32_e32 v19, v2
	v_mov_b32_e32 v20, v2
	v_mov_b32_e32 v21, v2
	.p2align 6
